# speedup vs baseline: 1.0065x; 1.0065x over previous
.LBB2_13:
	s_or_b64 exec, exec, s[10:11]
	v_mfma_f32_16x16x32_f16 v[92:95], v[42:45], v[34:37], 0
	v_cvt_f32_f16_e32 v89, v24
	v_lshlrev_b32_e32 v52, 3, v107
	s_movk_i32 s0, 0x50
	v_mfma_f32_16x16x32_f16 v[34:37], v[38:41], v[34:37], 0
	v_cvt_f32_f16_e32 v49, v108
	s_nop 2
	v_add_f32_e32 v24, v92, v134
	v_min_f32_e32 v46, 0x42a00000, v24
	v_mul_f32_e32 v46, 0x3fb8aa3b, v46
	v_exp_f32_e32 v46, v46
	v_add_f32_e32 v48, v93, v134
	v_min_f32_e32 v50, 0x42a00000, v48
	v_mul_f32_e32 v50, 0x3fb8aa3b, v50
	v_add_f32_e32 v46, 1.0, v46
	v_log_f32_e32 v46, v46
	v_exp_f32_e32 v50, v50
	v_add_f32_e32 v56, v95, v134
	v_min_f32_e32 v58, 0x42a00000, v56
	v_mul_f32_e32 v46, 0x3f317218, v46
	v_max_f32_e32 v24, v24, v46
	v_add_f32_e32 v46, 1.0, v50
	v_add_f32_e32 v50, v94, v134
	v_min_f32_e32 v54, 0x42a00000, v50
	v_mul_f32_e32 v54, 0x3fb8aa3b, v54
	v_exp_f32_e32 v54, v54
	v_mul_f32_e32 v58, 0x3fb8aa3b, v58
	v_exp_f32_e32 v58, v58
	v_log_f32_e32 v46, v46
	v_add_f32_e32 v54, 1.0, v54
	v_log_f32_e32 v54, v54
	v_add_f32_e32 v58, 1.0, v58
	v_log_f32_e32 v58, v58
	v_mul_f32_e32 v46, 0x3f317218, v46
	v_mfma_f32_16x16x32_f16 v[92:95], v[42:45], v[30:33], 0
	v_max_f32_e32 v46, v48, v46
	v_mul_f32_e32 v48, 0x3f317218, v54
	v_max_f32_e32 v48, v50, v48
	v_mul_f32_e32 v50, 0x3f317218, v58
	v_max_f32_e32 v50, v56, v50
	v_cvt_pk_f16_f32 v97, v48, v50
	s_nop 1
	v_add_f32_e32 v48, v92, v133
	v_min_f32_e32 v50, 0x42a00000, v48
	v_mul_f32_e32 v50, 0x3fb8aa3b, v50
	v_exp_f32_e32 v50, v50
	v_cvt_pk_f16_f32 v96, v24, v46
	v_add_f32_e32 v58, v95, v133
	v_min_f32_e32 v60, 0x42a00000, v58
	v_add_f32_e32 v46, 1.0, v50
	v_add_f32_e32 v50, v93, v133
	v_min_f32_e32 v54, 0x42a00000, v50
	v_log_f32_e32 v46, v46
	v_mul_f32_e32 v54, 0x3fb8aa3b, v54
	v_exp_f32_e32 v54, v54
	v_mul_f32_e32 v60, 0x3fb8aa3b, v60
	v_mul_f32_e32 v46, 0x3f317218, v46
	v_max_f32_e32 v46, v48, v46
	v_add_f32_e32 v48, 1.0, v54
	v_add_f32_e32 v54, v94, v133
	v_min_f32_e32 v56, 0x42a00000, v54
	v_mul_f32_e32 v56, 0x3fb8aa3b, v56
	v_exp_f32_e32 v56, v56
	v_exp_f32_e32 v60, v60
	v_log_f32_e32 v48, v48
	s_waitcnt vmcnt(9)
	v_mfma_f32_16x16x32_f16 v[92:95], v[42:45], v[26:29], 0
	v_add_f32_e32 v56, 1.0, v56
	v_log_f32_e32 v56, v56
	v_add_f32_e32 v60, 1.0, v60
	v_log_f32_e32 v60, v60
	v_mul_f32_e32 v48, 0x3f317218, v48
	v_max_f32_e32 v48, v50, v48
	v_mul_f32_e32 v50, 0x3f317218, v56
	s_nop 0
	v_add_f32_e32 v56, v92, v131
	v_max_f32_e32 v50, v54, v50
	v_mul_f32_e32 v54, 0x3f317218, v60
	v_min_f32_e32 v60, 0x42a00000, v56
	v_mul_f32_e32 v60, 0x3fb8aa3b, v60
	v_exp_f32_e32 v60, v60
	v_mad_u32_u24 v24, v136, s0, v52
	ds_write_b64 v24, v[96:97]
	v_cvt_pk_f16_f32 v96, v46, v48
	v_add_f32_e32 v46, 1.0, v60
	v_log_f32_e32 v46, v46
	v_max_f32_e32 v54, v58, v54
	v_add_f32_e32 v48, v93, v131
	v_cvt_pk_f16_f32 v97, v50, v54
	v_min_f32_e32 v50, 0x42a00000, v48
	v_mul_f32_e32 v46, 0x3f317218, v46
	v_add_f32_e32 v54, v94, v131
	v_mul_f32_e32 v50, 0x3fb8aa3b, v50
	v_max_f32_e32 v46, v56, v46
	v_min_f32_e32 v56, 0x42a00000, v54
	v_exp_f32_e32 v50, v50
	v_mul_f32_e32 v56, 0x3fb8aa3b, v56
	v_exp_f32_e32 v56, v56
	s_waitcnt vmcnt(8)
	v_mfma_f32_16x16x32_f16 v[42:45], v[42:45], v[18:21], 0
	v_add_f32_e32 v50, 1.0, v50
	v_log_f32_e32 v50, v50
	v_add_f32_e32 v56, 1.0, v56
	v_log_f32_e32 v56, v56
	v_add_f32_e32 v58, v95, v131
	v_mul_f32_e32 v50, 0x3f317218, v50
	s_nop 1
	v_add_f32_e32 v42, v42, v121
	v_min_f32_e32 v60, 0x42a00000, v58
	v_max_f32_e32 v48, v48, v50
	v_mul_f32_e32 v50, 0x3f317218, v56
	v_min_f32_e32 v56, 0x42a00000, v42
	v_mul_f32_e32 v60, 0x3fb8aa3b, v60
	v_mul_f32_e32 v56, 0x3fb8aa3b, v56
	v_exp_f32_e32 v60, v60
	v_exp_f32_e32 v56, v56
	v_add_f32_e32 v43, v43, v121
	v_cvt_pk_f16_f32 v92, v46, v48
	v_add_f32_e32 v60, 1.0, v60
	v_add_f32_e32 v46, 1.0, v56
	v_min_f32_e32 v48, 0x42a00000, v43
	v_log_f32_e32 v60, v60
	v_log_f32_e32 v46, v46
	v_mul_f32_e32 v48, 0x3fb8aa3b, v48
	v_exp_f32_e32 v48, v48
	v_max_f32_e32 v50, v54, v50
	v_mul_f32_e32 v54, 0x3f317218, v60
	v_mul_f32_e32 v46, 0x3f317218, v46
	v_add_f32_e32 v44, v44, v121
	v_max_f32_e32 v54, v58, v54
	v_max_f32_e32 v42, v42, v46
	v_add_f32_e32 v46, 1.0, v48
	v_min_f32_e32 v48, 0x42a00000, v44
	v_add_f32_e32 v45, v45, v121
	v_cvt_pk_f16_f32 v93, v50, v54
	v_mul_f32_e32 v48, 0x3fb8aa3b, v48
	v_min_f32_e32 v50, 0x42a00000, v45
	v_exp_f32_e32 v48, v48
	v_mul_f32_e32 v50, 0x3fb8aa3b, v50
	v_exp_f32_e32 v50, v50
	v_log_f32_e32 v46, v46
	v_add_f32_e32 v48, 1.0, v48
	v_log_f32_e32 v48, v48
	v_add_f32_e32 v50, 1.0, v50
	v_log_f32_e32 v50, v50
	v_mul_f32_e32 v46, 0x3f317218, v46
	v_max_f32_e32 v46, v43, v46
	v_mul_f32_e32 v43, 0x3f317218, v48
	v_max_f32_e32 v43, v44, v43
	v_mul_f32_e32 v44, 0x3f317218, v50
	v_add_f32_e32 v34, v34, v134
	v_max_f32_e32 v44, v45, v44
	v_min_f32_e32 v45, 0x42a00000, v34
	v_mul_f32_e32 v45, 0x3fb8aa3b, v45
	v_exp_f32_e32 v45, v45
	v_add_f32_e32 v35, v35, v134
	v_cvt_pk_f16_f32 v43, v43, v44
	v_cvt_pk_f16_f32 v42, v42, v46
	v_mad_u32_u24 v44, v135, s0, v52
	v_add_f32_e32 v45, 1.0, v45
	v_min_f32_e32 v46, 0x42a00000, v35
	v_add_f32_e32 v36, v36, v134
	ds_write_b64 v24, v[96:97] offset:1280
	ds_write_b64 v24, v[92:93] offset:2560
	v_log_f32_e32 v45, v45
	v_mul_f32_e32 v46, 0x3fb8aa3b, v46
	ds_write_b64 v44, v[42:43]
	v_min_f32_e32 v43, 0x42a00000, v36
	v_exp_f32_e32 v46, v46
	v_mul_f32_e32 v43, 0x3fb8aa3b, v43
	v_exp_f32_e32 v43, v43
	v_add_f32_e32 v37, v37, v134
	v_mul_f32_e32 v42, 0x3f317218, v45
	v_min_f32_e32 v45, 0x42a00000, v37
	v_max_f32_e32 v34, v34, v42
	v_add_f32_e32 v42, 1.0, v46
	v_mul_f32_e32 v45, 0x3fb8aa3b, v45
	v_log_f32_e32 v42, v42
	v_exp_f32_e32 v45, v45
	v_add_f32_e32 v43, 1.0, v43
	v_mfma_f32_16x16x32_f16 v[30:33], v[38:41], v[30:33], 0
	v_log_f32_e32 v43, v43
	v_mul_f32_e32 v42, 0x3f317218, v42
	v_add_f32_e32 v45, 1.0, v45
	v_log_f32_e32 v45, v45
	v_max_f32_e32 v42, v35, v42
	s_nop 2
	v_add_f32_e32 v30, v30, v133
	v_mul_f32_e32 v35, 0x3f317218, v43
	v_min_f32_e32 v43, 0x42a00000, v30
	v_mul_f32_e32 v43, 0x3fb8aa3b, v43
	v_exp_f32_e32 v43, v43
	v_max_f32_e32 v35, v36, v35
	v_mul_f32_e32 v36, 0x3f317218, v45
	v_max_f32_e32 v36, v37, v36
	v_add_f32_e32 v31, v31, v133
	v_cvt_pk_f16_f32 v35, v35, v36
	v_cvt_pk_f16_f32 v34, v34, v42
	v_add_f32_e32 v36, 1.0, v43
	v_min_f32_e32 v37, 0x42a00000, v31
	v_add_f32_e32 v32, v32, v133
	v_log_f32_e32 v36, v36
	v_mul_f32_e32 v37, 0x3fb8aa3b, v37
	ds_write_b64 v24, v[34:35] offset:32
	v_min_f32_e32 v35, 0x42a00000, v32
	v_exp_f32_e32 v37, v37
	v_mul_f32_e32 v35, 0x3fb8aa3b, v35
	v_exp_f32_e32 v35, v35
	v_add_f32_e32 v33, v33, v133
	v_mul_f32_e32 v34, 0x3f317218, v36
	v_min_f32_e32 v36, 0x42a00000, v33
	v_max_f32_e32 v30, v30, v34
	v_add_f32_e32 v34, 1.0, v37
	v_mul_f32_e32 v36, 0x3fb8aa3b, v36
	v_log_f32_e32 v34, v34
	v_exp_f32_e32 v36, v36
	v_add_f32_e32 v35, 1.0, v35
	v_mfma_f32_16x16x32_f16 v[26:29], v[38:41], v[26:29], 0
	v_log_f32_e32 v35, v35
	v_mul_f32_e32 v34, 0x3f317218, v34
	v_add_f32_e32 v36, 1.0, v36
	v_log_f32_e32 v36, v36
	v_max_f32_e32 v34, v31, v34
	s_nop 2
	v_add_f32_e32 v26, v26, v131
	v_mul_f32_e32 v31, 0x3f317218, v35
	v_min_f32_e32 v35, 0x42a00000, v26
	v_mul_f32_e32 v35, 0x3fb8aa3b, v35
	v_exp_f32_e32 v35, v35
	v_max_f32_e32 v31, v32, v31
	v_mul_f32_e32 v32, 0x3f317218, v36
	v_max_f32_e32 v32, v33, v32
	v_add_f32_e32 v27, v27, v131
	v_cvt_pk_f16_f32 v31, v31, v32
	v_cvt_pk_f16_f32 v30, v30, v34
	v_add_f32_e32 v32, 1.0, v35
	v_min_f32_e32 v33, 0x42a00000, v27
	v_add_f32_e32 v28, v28, v131
	v_log_f32_e32 v32, v32
	v_mul_f32_e32 v33, 0x3fb8aa3b, v33
	ds_write_b64 v24, v[30:31] offset:1312
	v_min_f32_e32 v31, 0x42a00000, v28
	v_exp_f32_e32 v33, v33
	v_mul_f32_e32 v31, 0x3fb8aa3b, v31
	v_exp_f32_e32 v31, v31
	v_add_f32_e32 v29, v29, v131
	v_mul_f32_e32 v30, 0x3f317218, v32
	v_min_f32_e32 v32, 0x42a00000, v29
	v_max_f32_e32 v26, v26, v30
	v_add_f32_e32 v30, 1.0, v33
	v_mul_f32_e32 v32, 0x3fb8aa3b, v32
	v_log_f32_e32 v30, v30
	v_exp_f32_e32 v32, v32
	v_add_f32_e32 v31, 1.0, v31
	v_mfma_f32_16x16x32_f16 v[18:21], v[38:41], v[18:21], 0
	v_log_f32_e32 v31, v31
	v_mul_f32_e32 v30, 0x3f317218, v30
	v_add_f32_e32 v32, 1.0, v32
	v_log_f32_e32 v32, v32
	v_max_f32_e32 v30, v27, v30
	s_nop 2
	v_add_f32_e32 v18, v18, v121
	v_mul_f32_e32 v27, 0x3f317218, v31
	v_min_f32_e32 v31, 0x42a00000, v18
	v_mul_f32_e32 v31, 0x3fb8aa3b, v31
	v_exp_f32_e32 v31, v31
	v_max_f32_e32 v27, v28, v27
	v_mul_f32_e32 v28, 0x3f317218, v32
	v_max_f32_e32 v28, v29, v28
	v_add_f32_e32 v19, v19, v121
	v_cvt_pk_f16_f32 v27, v27, v28
	v_cvt_pk_f16_f32 v26, v26, v30
	v_add_f32_e32 v28, 1.0, v31
	v_min_f32_e32 v29, 0x42a00000, v19
	v_add_f32_e32 v20, v20, v121
	v_log_f32_e32 v28, v28
	v_mul_f32_e32 v29, 0x3fb8aa3b, v29
	ds_write_b64 v24, v[26:27] offset:2592
	v_min_f32_e32 v26, 0x42a00000, v20
	v_add_f32_e32 v21, v21, v121
	v_exp_f32_e32 v29, v29
	v_mul_f32_e32 v26, 0x3fb8aa3b, v26
	v_min_f32_e32 v27, 0x42a00000, v21
	v_exp_f32_e32 v26, v26
	v_mul_f32_e32 v27, 0x3fb8aa3b, v27
	v_exp_f32_e32 v27, v27
	v_mul_f32_e32 v24, 0x3f317218, v28
	v_max_f32_e32 v18, v18, v24
	v_add_f32_e32 v24, 1.0, v29
	v_log_f32_e32 v24, v24
	v_add_f32_e32 v26, 1.0, v26
	v_log_f32_e32 v26, v26
	v_add_f32_e32 v27, 1.0, v27
	v_log_f32_e32 v27, v27
	v_mul_f32_e32 v24, 0x3f317218, v24
	v_max_f32_e32 v24, v19, v24
	v_mul_f32_e32 v19, 0x3f317218, v26
	v_max_f32_e32 v19, v20, v19
	v_mul_f32_e32 v20, 0x3f317218, v27
	v_max_f32_e32 v20, v21, v20
	v_cvt_pk_f16_f32 v19, v19, v20
	v_cvt_pk_f16_f32 v18, v18, v24
	ds_write_b64 v44, v[18:19] offset:32
	v_mul_u32_u24_e32 v18, 0x50, v0
	s_waitcnt lgkmcnt(0)
	s_barrier
	ds_read_b128 v[92:95], v18
	v_cvt_f32_f16_e32 v55, v111
	v_cvt_f32_f16_e32 v59, v110
	v_cvt_f32_f16_e32 v79, v105
	v_cvt_f32_f16_e32 v82, v104
	v_cvt_f32_f16_e32 v84, v103
	v_cvt_f32_f16_e32 v86, v102
	ds_read_b128 v[96:99], v18 offset:16
	ds_read_b128 v[100:103], v18 offset:32
	ds_read_b128 v[108:111], v18 offset:48
	v_lshl_add_u64 v[104:105], s[8:9], 0, v[118:119]
	v_cvt_f32_f16_e32 v47, v113
	v_cvt_f32_f16_e32 v51, v112
	v_lshl_add_u64 v[112:113], v[104:105], 0, s[6:7]
	s_waitcnt lgkmcnt(3)
	v_cvt_f32_f16_e32 v26, v94
	v_cvt_f32_f16_sdwa v28, v94 dst_sel:DWORD dst_unused:UNUSED_PAD src0_sel:WORD_1
	v_cvt_f32_f16_e32 v30, v95
	v_cvt_f32_f16_sdwa v32, v95 dst_sel:DWORD dst_unused:UNUSED_PAD src0_sel:WORD_1
	global_store_dwordx4 v[112:113], v[92:95], off sc0 sc1
	v_cvt_f32_f16_e32 v53, v122
	v_cvt_f32_f16_e32 v57, v125
	v_lshl_add_u64 v[94:95], v[104:105], 0, s[14:15]
	s_waitcnt lgkmcnt(2)
	global_store_dwordx4 v[94:95], v[96:99], off sc0 sc1
	v_lshl_add_u64 v[94:95], v[104:105], 0, s[16:17]
	s_waitcnt lgkmcnt(1)
	global_store_dwordx4 v[94:95], v[100:103], off sc0 sc1
	v_lshl_add_u64 v[94:95], v[104:105], 0, s[18:19]
	v_cvt_f32_f16_e32 v61, v124
	v_cvt_f32_f16_e32 v63, v117
	v_cvt_f32_f16_e32 v65, v147
	v_cvt_f32_f16_e32 v67, v116
	v_cvt_f32_f16_e32 v69, v145
	v_cvt_f32_f16_e32 v71, v115
	v_cvt_f32_f16_e32 v73, v127
	v_cvt_f32_f16_e32 v75, v114
	v_cvt_f32_f16_e32 v77, v126
	v_cvt_f32_f16_e32 v81, v142
	v_cvt_f32_f16_e32 v83, v141
	v_cvt_f32_f16_e32 v85, v140
	v_cvt_f32_f16_e32 v87, v139
	v_cvt_f32_f16_e32 v25, v25
	v_cvt_f32_f16_e32 v88, v138
	v_cvt_f32_f16_e32 v90, v137
	v_cvt_f32_f16_e32 v23, v23
	v_cvt_f32_f16_e32 v91, v123
	v_cvt_f32_f16_e32 v19, v22
	v_cvt_f32_f16_sdwa v20, v92 dst_sel:DWORD dst_unused:UNUSED_PAD src0_sel:WORD_1
	v_cvt_f32_f16_e32 v22, v93
	v_cvt_f32_f16_sdwa v24, v93 dst_sel:DWORD dst_unused:UNUSED_PAD src0_sel:WORD_1
	v_cvt_f32_f16_e32 v34, v96
	v_cvt_f32_f16_sdwa v36, v96 dst_sel:DWORD dst_unused:UNUSED_PAD src0_sel:WORD_1
	v_cvt_f32_f16_e32 v38, v97
	v_cvt_f32_f16_sdwa v40, v97 dst_sel:DWORD dst_unused:UNUSED_PAD src0_sel:WORD_1
	v_cvt_f32_f16_e32 v42, v98
	v_cvt_f32_f16_sdwa v44, v98 dst_sel:DWORD dst_unused:UNUSED_PAD src0_sel:WORD_1
	v_cvt_f32_f16_e32 v46, v99
	v_cvt_f32_f16_sdwa v48, v99 dst_sel:DWORD dst_unused:UNUSED_PAD src0_sel:WORD_1
	v_cvt_f32_f16_e32 v50, v100
	v_cvt_f32_f16_sdwa v52, v100 dst_sel:DWORD dst_unused:UNUSED_PAD src0_sel:WORD_1
	v_cvt_f32_f16_e32 v54, v101
	v_cvt_f32_f16_sdwa v56, v101 dst_sel:DWORD dst_unused:UNUSED_PAD src0_sel:WORD_1
	v_cvt_f32_f16_e32 v58, v102
	v_cvt_f32_f16_sdwa v60, v102 dst_sel:DWORD dst_unused:UNUSED_PAD src0_sel:WORD_1
	v_cvt_f32_f16_e32 v62, v103
	v_cvt_f32_f16_sdwa v64, v103 dst_sel:DWORD dst_unused:UNUSED_PAD src0_sel:WORD_1
	s_waitcnt lgkmcnt(0)
	v_cvt_f32_f16_e32 v66, v108
	v_cvt_f32_f16_sdwa v68, v108 dst_sel:DWORD dst_unused:UNUSED_PAD src0_sel:WORD_1
	v_cvt_f32_f16_e32 v70, v109
	v_cvt_f32_f16_sdwa v72, v109 dst_sel:DWORD dst_unused:UNUSED_PAD src0_sel:WORD_1
	v_cvt_f32_f16_e32 v74, v110
	v_cvt_f32_f16_sdwa v76, v110 dst_sel:DWORD dst_unused:UNUSED_PAD src0_sel:WORD_1
	v_cvt_f32_f16_e32 v78, v111
	v_cvt_f32_f16_sdwa v18, v111 dst_sel:DWORD dst_unused:UNUSED_PAD src0_sel:WORD_1
	global_store_dwordx4 v[94:95], v[108:111], off sc0 sc1
	v_cvt_f32_f16_e32 v80, v92
	v_mov_b32_e32 v21, 0xa000
	v_mov_b32_e32 v27, 0xa0d0
	ds_read_b128 v[92:95], v21 offset:64
	ds_read_b128 v[96:99], v21 offset:80
	ds_read_b128 v[100:103], v21 offset:96
	ds_read_b128 v[108:111], v21 offset:112
	s_waitcnt lgkmcnt(0)
	ds_read_b128 v[112:115], v27 offset:64
	ds_read_b128 v[116:119], v27 offset:80
	ds_read_b128 v[120:123], v27 offset:96
	ds_read_b128 v[124:127], v27 offset:112
	s_lshr_b32 s0, s23, 5
	s_waitcnt vmcnt(11)
	v_mul_f32_e32 v104, v80, v19
	v_pk_mul_f32 v[128:129], v[104:105], v[92:93] op_sel_hi:[0,1]
	v_pk_mul_f32 v[130:131], v[104:105], v[94:95] op_sel_hi:[0,1]
	s_waitcnt vmcnt(10)
	v_pk_mul_f32 v[132:133], v[104:105], v[96:97] op_sel_hi:[0,1]
	v_pk_mul_f32 v[134:135], v[104:105], v[98:99] op_sel_hi:[0,1]
	s_waitcnt vmcnt(9)
	v_pk_mul_f32 v[136:137], v[104:105], v[100:101] op_sel_hi:[0,1]
	v_pk_mul_f32 v[138:139], v[104:105], v[102:103] op_sel_hi:[0,1]
	s_waitcnt vmcnt(8)
	v_pk_mul_f32 v[140:141], v[104:105], v[108:109] op_sel_hi:[0,1]
	v_pk_mul_f32 v[104:105], v[104:105], v[110:111] op_sel_hi:[0,1]
	v_mov_b32_e32 v19, 0xa1a0
	s_waitcnt lgkmcnt(0)
	s_and_b32 s6, s22, 0x7ffffc0
	ds_read_b128 v[92:95], v19 offset:64
	ds_read_b128 v[96:99], v19 offset:80
	ds_read_b128 v[100:103], v19 offset:96
	ds_read_b128 v[108:111], v19 offset:112
	v_mov_b32_e32 v19, 0xa270
	v_pk_mul_f32 v[142:143], v[20:21], v[14:15] op_sel_hi:[0,1]
	v_exp_f32_e32 v142, v142
	v_exp_f32_e32 v143, v143
	v_mul_f32_e32 v144, v20, v91
	v_pk_mul_f32 v[112:113], v[144:145], v[112:113] op_sel_hi:[0,1]
	v_pk_mul_f32 v[114:115], v[144:145], v[114:115] op_sel_hi:[0,1]
	v_pk_fma_f32 v[128:129], v[128:129], v[142:143], v[112:113]
	v_pk_mul_f32 v[112:113], v[20:21], v[16:17] op_sel_hi:[0,1]
	v_exp_f32_e32 v112, v112
	v_exp_f32_e32 v113, v113
	v_pk_mul_f32 v[116:117], v[144:145], v[116:117] op_sel_hi:[0,1]
	s_or_b32 s0, s0, s6
	s_lshl_b64 s[6:7], s[0:1], 14
	v_pk_fma_f32 v[130:131], v[130:131], v[112:113], v[114:115]
	v_pk_mul_f32 v[112:113], v[20:21], v[10:11] op_sel_hi:[0,1]
	v_exp_f32_e32 v112, v112
	v_exp_f32_e32 v113, v113
	v_pk_mul_f32 v[114:115], v[20:21], v[12:13] op_sel_hi:[0,1]
	v_exp_f32_e32 v114, v114
	v_exp_f32_e32 v115, v115
	v_pk_fma_f32 v[132:133], v[132:133], v[112:113], v[116:117]
	v_pk_mul_f32 v[112:113], v[144:145], v[118:119] op_sel_hi:[0,1]
	v_pk_mul_f32 v[116:117], v[144:145], v[120:121] op_sel_hi:[0,1]
	v_pk_fma_f32 v[134:135], v[134:135], v[114:115], v[112:113]
	v_pk_mul_f32 v[112:113], v[20:21], v[6:7] op_sel_hi:[0,1]
	v_exp_f32_e32 v112, v112
	v_exp_f32_e32 v113, v113
	v_pk_mul_f32 v[114:115], v[20:21], v[8:9] op_sel_hi:[0,1]
	v_exp_f32_e32 v114, v114
	v_exp_f32_e32 v115, v115
	v_pk_fma_f32 v[136:137], v[136:137], v[112:113], v[116:117]
	v_pk_mul_f32 v[112:113], v[144:145], v[122:123] op_sel_hi:[0,1]
	v_pk_mul_f32 v[116:117], v[144:145], v[124:125] op_sel_hi:[0,1]
	v_pk_fma_f32 v[138:139], v[138:139], v[114:115], v[112:113]
	v_pk_mul_f32 v[112:113], v[20:21], v[2:3] op_sel_hi:[0,1]
	v_exp_f32_e32 v112, v112
	v_exp_f32_e32 v113, v113
	v_pk_mul_f32 v[114:115], v[20:21], v[4:5] op_sel_hi:[0,1]
	v_exp_f32_e32 v114, v114
	v_exp_f32_e32 v115, v115
	v_pk_fma_f32 v[140:141], v[140:141], v[112:113], v[116:117]
	v_pk_mul_f32 v[112:113], v[144:145], v[126:127] op_sel_hi:[0,1]
	s_lshl_b64 s[0:1], s[0:1], 11
	v_pk_fma_f32 v[104:105], v[104:105], v[114:115], v[112:113]
	s_add_u32 s0, s2, s0
	s_waitcnt lgkmcnt(0)
	s_addc_u32 s1, s3, s1
	ds_read_b128 v[112:115], v19 offset:64
	ds_read_b128 v[116:119], v19 offset:80
	ds_read_b128 v[120:123], v19 offset:96
	ds_read_b128 v[124:127], v19 offset:112
	v_mov_b32_e32 v19, 0xa340
	v_pk_mul_f32 v[142:143], v[22:23], v[14:15] op_sel_hi:[0,1]
	v_exp_f32_e32 v142, v142
	v_exp_f32_e32 v143, v143
	v_mul_f32_e32 v144, v22, v23
	v_pk_mul_f32 v[92:93], v[144:145], v[92:93] op_sel_hi:[0,1]
	v_pk_mul_f32 v[94:95], v[144:145], v[94:95] op_sel_hi:[0,1]
	v_pk_fma_f32 v[128:129], v[128:129], v[142:143], v[92:93]
	v_pk_mul_f32 v[92:93], v[22:23], v[16:17] op_sel_hi:[0,1]
	v_exp_f32_e32 v92, v92
	v_exp_f32_e32 v93, v93
	v_pk_mul_f32 v[96:97], v[144:145], v[96:97] op_sel_hi:[0,1]
	v_pk_fma_f32 v[130:131], v[130:131], v[92:93], v[94:95]
	v_pk_mul_f32 v[92:93], v[22:23], v[10:11] op_sel_hi:[0,1]
	v_exp_f32_e32 v92, v92
	v_exp_f32_e32 v93, v93
	v_pk_mul_f32 v[94:95], v[22:23], v[12:13] op_sel_hi:[0,1]
	v_exp_f32_e32 v94, v94
	v_exp_f32_e32 v95, v95
	v_pk_fma_f32 v[132:133], v[132:133], v[92:93], v[96:97]
	v_pk_mul_f32 v[92:93], v[144:145], v[98:99] op_sel_hi:[0,1]
	v_pk_mul_f32 v[96:97], v[144:145], v[100:101] op_sel_hi:[0,1]
	v_pk_fma_f32 v[134:135], v[134:135], v[94:95], v[92:93]
	v_pk_mul_f32 v[92:93], v[22:23], v[6:7] op_sel_hi:[0,1]
	v_exp_f32_e32 v92, v92
	v_exp_f32_e32 v93, v93
	v_pk_mul_f32 v[94:95], v[22:23], v[8:9] op_sel_hi:[0,1]
	v_exp_f32_e32 v94, v94
	v_exp_f32_e32 v95, v95
	v_pk_fma_f32 v[136:137], v[136:137], v[92:93], v[96:97]
	v_pk_mul_f32 v[92:93], v[144:145], v[102:103] op_sel_hi:[0,1]
	v_pk_mul_f32 v[96:97], v[144:145], v[108:109] op_sel_hi:[0,1]
	v_pk_fma_f32 v[138:139], v[138:139], v[94:95], v[92:93]
	v_pk_mul_f32 v[92:93], v[22:23], v[2:3] op_sel_hi:[0,1]
	v_exp_f32_e32 v92, v92
	v_exp_f32_e32 v93, v93
	v_pk_mul_f32 v[94:95], v[22:23], v[4:5] op_sel_hi:[0,1]
	v_exp_f32_e32 v94, v94
	v_exp_f32_e32 v95, v95
	v_pk_fma_f32 v[140:141], v[140:141], v[92:93], v[96:97]
	v_pk_mul_f32 v[92:93], v[144:145], v[110:111] op_sel_hi:[0,1]
	v_pk_fma_f32 v[104:105], v[104:105], v[94:95], v[92:93]
	s_nop 0
	s_waitcnt lgkmcnt(0)
	s_nop 0
	ds_read_b128 v[92:95], v19 offset:64
	ds_read_b128 v[96:99], v19 offset:80
	ds_read_b128 v[100:103], v19 offset:96
	ds_read_b128 v[108:111], v19 offset:112
	v_mov_b32_e32 v19, 0xa410
	v_pk_mul_f32 v[142:143], v[24:25], v[14:15] op_sel_hi:[0,1]
	v_exp_f32_e32 v142, v142
	v_exp_f32_e32 v143, v143
	v_mul_f32_e32 v90, v24, v90
	v_pk_mul_f32 v[112:113], v[90:91], v[112:113] op_sel_hi:[0,1]
	v_pk_mul_f32 v[114:115], v[90:91], v[114:115] op_sel_hi:[0,1]
	v_pk_fma_f32 v[128:129], v[128:129], v[142:143], v[112:113]
	v_pk_mul_f32 v[112:113], v[24:25], v[16:17] op_sel_hi:[0,1]
	v_exp_f32_e32 v112, v112
	v_exp_f32_e32 v113, v113
	v_pk_mul_f32 v[116:117], v[90:91], v[116:117] op_sel_hi:[0,1]
	v_pk_fma_f32 v[130:131], v[130:131], v[112:113], v[114:115]
	v_pk_mul_f32 v[112:113], v[24:25], v[10:11] op_sel_hi:[0,1]
	v_exp_f32_e32 v112, v112
	v_exp_f32_e32 v113, v113
	v_pk_mul_f32 v[114:115], v[24:25], v[12:13] op_sel_hi:[0,1]
	v_exp_f32_e32 v114, v114
	v_exp_f32_e32 v115, v115
	v_pk_fma_f32 v[132:133], v[132:133], v[112:113], v[116:117]
	v_pk_mul_f32 v[112:113], v[90:91], v[118:119] op_sel_hi:[0,1]
	v_pk_mul_f32 v[116:117], v[90:91], v[120:121] op_sel_hi:[0,1]
	v_pk_fma_f32 v[134:135], v[134:135], v[114:115], v[112:113]
	v_pk_mul_f32 v[112:113], v[24:25], v[6:7] op_sel_hi:[0,1]
	v_exp_f32_e32 v112, v112
	v_exp_f32_e32 v113, v113
	v_pk_mul_f32 v[114:115], v[24:25], v[8:9] op_sel_hi:[0,1]
	v_exp_f32_e32 v114, v114
	v_exp_f32_e32 v115, v115
	v_pk_fma_f32 v[136:137], v[136:137], v[112:113], v[116:117]
	v_pk_mul_f32 v[112:113], v[90:91], v[122:123] op_sel_hi:[0,1]
	v_pk_mul_f32 v[116:117], v[90:91], v[124:125] op_sel_hi:[0,1]
	v_pk_fma_f32 v[138:139], v[138:139], v[114:115], v[112:113]
	v_pk_mul_f32 v[112:113], v[24:25], v[2:3] op_sel_hi:[0,1]
	v_pk_mul_f32 v[114:115], v[24:25], v[4:5] op_sel_hi:[0,1]
	v_exp_f32_e32 v112, v112
	v_exp_f32_e32 v113, v113
	v_exp_f32_e32 v114, v114
	v_exp_f32_e32 v115, v115
	v_pk_mul_f32 v[90:91], v[90:91], v[126:127] op_sel_hi:[0,1]
	v_pk_fma_f32 v[140:141], v[140:141], v[112:113], v[116:117]
	v_pk_fma_f32 v[90:91], v[104:105], v[114:115], v[90:91]
	s_nop 0
	s_waitcnt lgkmcnt(0)
	s_nop 0
	ds_read_b128 v[112:115], v19 offset:64
	ds_read_b128 v[116:119], v19 offset:80
	ds_read_b128 v[120:123], v19 offset:96
	ds_read_b128 v[124:127], v19 offset:112
	v_mov_b32_e32 v19, 0xa4e0
	v_pk_mul_f32 v[104:105], v[26:27], v[14:15] op_sel_hi:[0,1]
	v_exp_f32_e32 v104, v104
	v_exp_f32_e32 v105, v105
	v_mul_f32_e32 v142, v26, v89
	v_pk_mul_f32 v[92:93], v[142:143], v[92:93] op_sel_hi:[0,1]
	v_pk_mul_f32 v[94:95], v[142:143], v[94:95] op_sel_hi:[0,1]
	v_pk_fma_f32 v[128:129], v[128:129], v[104:105], v[92:93]
	v_pk_mul_f32 v[92:93], v[26:27], v[16:17] op_sel_hi:[0,1]
	v_exp_f32_e32 v92, v92
	v_exp_f32_e32 v93, v93
	v_pk_mul_f32 v[96:97], v[142:143], v[96:97] op_sel_hi:[0,1]
	v_pk_fma_f32 v[130:131], v[130:131], v[92:93], v[94:95]
	v_pk_mul_f32 v[92:93], v[26:27], v[10:11] op_sel_hi:[0,1]
	v_exp_f32_e32 v92, v92
	v_exp_f32_e32 v93, v93
	v_pk_mul_f32 v[94:95], v[26:27], v[12:13] op_sel_hi:[0,1]
	v_exp_f32_e32 v94, v94
	v_exp_f32_e32 v95, v95
	v_pk_fma_f32 v[132:133], v[132:133], v[92:93], v[96:97]
	v_pk_mul_f32 v[92:93], v[142:143], v[98:99] op_sel_hi:[0,1]
	v_pk_mul_f32 v[96:97], v[142:143], v[100:101] op_sel_hi:[0,1]
	v_pk_fma_f32 v[134:135], v[134:135], v[94:95], v[92:93]
	v_pk_mul_f32 v[92:93], v[26:27], v[6:7] op_sel_hi:[0,1]
	v_exp_f32_e32 v92, v92
	v_exp_f32_e32 v93, v93
	v_pk_mul_f32 v[94:95], v[26:27], v[8:9] op_sel_hi:[0,1]
	v_exp_f32_e32 v94, v94
	v_exp_f32_e32 v95, v95
	v_pk_fma_f32 v[136:137], v[136:137], v[92:93], v[96:97]
	v_pk_mul_f32 v[92:93], v[142:143], v[102:103] op_sel_hi:[0,1]
	v_pk_mul_f32 v[96:97], v[142:143], v[108:109] op_sel_hi:[0,1]
	v_pk_fma_f32 v[138:139], v[138:139], v[94:95], v[92:93]
	v_pk_mul_f32 v[92:93], v[26:27], v[2:3] op_sel_hi:[0,1]
	v_exp_f32_e32 v92, v92
	v_exp_f32_e32 v93, v93
	v_pk_mul_f32 v[94:95], v[26:27], v[4:5] op_sel_hi:[0,1]
	v_exp_f32_e32 v94, v94
	v_exp_f32_e32 v95, v95
	v_pk_fma_f32 v[108:109], v[140:141], v[92:93], v[96:97]
	v_pk_mul_f32 v[92:93], v[142:143], v[110:111] op_sel_hi:[0,1]
	v_pk_fma_f32 v[110:111], v[90:91], v[94:95], v[92:93]
	s_nop 0
	s_waitcnt lgkmcnt(0)
	s_nop 0
	ds_read_b128 v[90:93], v19 offset:64
	ds_read_b128 v[94:97], v19 offset:80
	ds_read_b128 v[98:101], v19 offset:96
	ds_read_b128 v[102:105], v19 offset:112
	v_mov_b32_e32 v19, 0xa5b0
	v_pk_mul_f32 v[140:141], v[28:29], v[14:15] op_sel_hi:[0,1]
	v_exp_f32_e32 v140, v140
	v_exp_f32_e32 v141, v141
	v_pk_mul_f32 v[142:143], v[28:29], v[16:17] op_sel_hi:[0,1]
	v_exp_f32_e32 v142, v142
	v_exp_f32_e32 v143, v143
	v_mul_f32_e32 v88, v28, v88
	v_pk_mul_f32 v[112:113], v[88:89], v[112:113] op_sel_hi:[0,1]
	v_pk_fma_f32 v[128:129], v[128:129], v[140:141], v[112:113]
	v_pk_mul_f32 v[112:113], v[88:89], v[114:115] op_sel_hi:[0,1]
	v_pk_fma_f32 v[130:131], v[130:131], v[142:143], v[112:113]
	v_pk_mul_f32 v[112:113], v[28:29], v[10:11] op_sel_hi:[0,1]
	v_exp_f32_e32 v112, v112
	v_exp_f32_e32 v113, v113
	v_pk_mul_f32 v[114:115], v[28:29], v[12:13] op_sel_hi:[0,1]
	v_exp_f32_e32 v114, v114
	v_exp_f32_e32 v115, v115
	v_pk_mul_f32 v[116:117], v[88:89], v[116:117] op_sel_hi:[0,1]
	v_pk_fma_f32 v[132:133], v[132:133], v[112:113], v[116:117]
	v_pk_mul_f32 v[112:113], v[88:89], v[118:119] op_sel_hi:[0,1]
	v_pk_fma_f32 v[134:135], v[134:135], v[114:115], v[112:113]
	v_pk_mul_f32 v[112:113], v[28:29], v[6:7] op_sel_hi:[0,1]
	v_exp_f32_e32 v112, v112
	v_exp_f32_e32 v113, v113
	v_pk_mul_f32 v[114:115], v[28:29], v[8:9] op_sel_hi:[0,1]
	v_exp_f32_e32 v114, v114
	v_exp_f32_e32 v115, v115
	v_pk_mul_f32 v[116:117], v[88:89], v[120:121] op_sel_hi:[0,1]
	v_pk_fma_f32 v[136:137], v[136:137], v[112:113], v[116:117]
	v_pk_mul_f32 v[112:113], v[88:89], v[122:123] op_sel_hi:[0,1]
	v_pk_fma_f32 v[138:139], v[138:139], v[114:115], v[112:113]
	v_pk_mul_f32 v[112:113], v[28:29], v[2:3] op_sel_hi:[0,1]
	v_pk_mul_f32 v[114:115], v[28:29], v[4:5] op_sel_hi:[0,1]
	v_exp_f32_e32 v112, v112
	v_exp_f32_e32 v113, v113
	v_exp_f32_e32 v114, v114
	v_exp_f32_e32 v115, v115
	v_pk_mul_f32 v[116:117], v[88:89], v[124:125] op_sel_hi:[0,1]
	v_pk_mul_f32 v[88:89], v[88:89], v[126:127] op_sel_hi:[0,1]
	v_pk_fma_f32 v[124:125], v[108:109], v[112:113], v[116:117]
	v_pk_fma_f32 v[88:89], v[110:111], v[114:115], v[88:89]
	s_nop 0
	s_waitcnt lgkmcnt(0)
	s_nop 0
	ds_read_b128 v[108:111], v19 offset:64
	ds_read_b128 v[112:115], v19 offset:80
	ds_read_b128 v[116:119], v19 offset:96
	ds_read_b128 v[120:123], v19 offset:112
	v_mov_b32_e32 v19, 0xa680
	v_pk_mul_f32 v[140:141], v[30:31], v[14:15] op_sel_hi:[0,1]
	v_exp_f32_e32 v140, v140
	v_exp_f32_e32 v141, v141
	v_pk_mul_f32 v[142:143], v[30:31], v[16:17] op_sel_hi:[0,1]
	v_exp_f32_e32 v142, v142
	v_exp_f32_e32 v143, v143
	v_mul_f32_e32 v126, v30, v25
	v_pk_mul_f32 v[90:91], v[126:127], v[90:91] op_sel_hi:[0,1]
	v_pk_fma_f32 v[128:129], v[128:129], v[140:141], v[90:91]
	v_pk_mul_f32 v[90:91], v[126:127], v[92:93] op_sel_hi:[0,1]
	v_pk_fma_f32 v[130:131], v[130:131], v[142:143], v[90:91]
	v_pk_mul_f32 v[90:91], v[30:31], v[10:11] op_sel_hi:[0,1]
	v_exp_f32_e32 v90, v90
	v_exp_f32_e32 v91, v91
	v_pk_mul_f32 v[92:93], v[30:31], v[12:13] op_sel_hi:[0,1]
	v_exp_f32_e32 v92, v92
	v_exp_f32_e32 v93, v93
	v_pk_mul_f32 v[94:95], v[126:127], v[94:95] op_sel_hi:[0,1]
	v_pk_fma_f32 v[132:133], v[132:133], v[90:91], v[94:95]
	v_pk_mul_f32 v[90:91], v[126:127], v[96:97] op_sel_hi:[0,1]
	v_pk_fma_f32 v[134:135], v[134:135], v[92:93], v[90:91]
	v_pk_mul_f32 v[90:91], v[30:31], v[6:7] op_sel_hi:[0,1]
	v_exp_f32_e32 v90, v90
	v_exp_f32_e32 v91, v91
	v_pk_mul_f32 v[92:93], v[30:31], v[8:9] op_sel_hi:[0,1]
	v_exp_f32_e32 v92, v92
	v_exp_f32_e32 v93, v93
	v_pk_mul_f32 v[94:95], v[126:127], v[98:99] op_sel_hi:[0,1]
	v_pk_fma_f32 v[136:137], v[136:137], v[90:91], v[94:95]
	v_pk_mul_f32 v[90:91], v[126:127], v[100:101] op_sel_hi:[0,1]
	v_pk_fma_f32 v[138:139], v[138:139], v[92:93], v[90:91]
	v_pk_mul_f32 v[90:91], v[30:31], v[2:3] op_sel_hi:[0,1]
	v_exp_f32_e32 v90, v90
	v_exp_f32_e32 v91, v91
	v_pk_mul_f32 v[92:93], v[30:31], v[4:5] op_sel_hi:[0,1]
	v_exp_f32_e32 v92, v92
	v_exp_f32_e32 v93, v93
	v_pk_mul_f32 v[94:95], v[126:127], v[102:103] op_sel_hi:[0,1]
	v_pk_fma_f32 v[124:125], v[124:125], v[90:91], v[94:95]
	v_pk_mul_f32 v[90:91], v[126:127], v[104:105] op_sel_hi:[0,1]
	v_pk_fma_f32 v[104:105], v[88:89], v[92:93], v[90:91]
	s_nop 0
	s_waitcnt lgkmcnt(0)
	s_nop 0
	ds_read_b128 v[88:91], v19 offset:64
	ds_read_b128 v[92:95], v19 offset:80
	ds_read_b128 v[96:99], v19 offset:96
	ds_read_b128 v[100:103], v19 offset:112
	v_mov_b32_e32 v19, 0xa750
	v_pk_mul_f32 v[140:141], v[32:33], v[14:15] op_sel_hi:[0,1]
	v_exp_f32_e32 v140, v140
	v_exp_f32_e32 v141, v141
	v_pk_mul_f32 v[142:143], v[32:33], v[16:17] op_sel_hi:[0,1]
	v_exp_f32_e32 v142, v142
	v_exp_f32_e32 v143, v143
	v_mul_f32_e32 v126, v32, v87
	v_pk_mul_f32 v[108:109], v[126:127], v[108:109] op_sel_hi:[0,1]
	v_pk_fma_f32 v[128:129], v[128:129], v[140:141], v[108:109]
	v_pk_mul_f32 v[108:109], v[126:127], v[110:111] op_sel_hi:[0,1]
	v_pk_fma_f32 v[130:131], v[130:131], v[142:143], v[108:109]
	v_pk_mul_f32 v[108:109], v[32:33], v[10:11] op_sel_hi:[0,1]
	v_exp_f32_e32 v108, v108
	v_exp_f32_e32 v109, v109
	v_pk_mul_f32 v[110:111], v[32:33], v[12:13] op_sel_hi:[0,1]
	v_exp_f32_e32 v110, v110
	v_exp_f32_e32 v111, v111
	v_pk_mul_f32 v[112:113], v[126:127], v[112:113] op_sel_hi:[0,1]
	v_pk_fma_f32 v[132:133], v[132:133], v[108:109], v[112:113]
	v_pk_mul_f32 v[108:109], v[126:127], v[114:115] op_sel_hi:[0,1]
	v_pk_fma_f32 v[134:135], v[134:135], v[110:111], v[108:109]
	v_pk_mul_f32 v[108:109], v[32:33], v[6:7] op_sel_hi:[0,1]
	v_exp_f32_e32 v108, v108
	v_exp_f32_e32 v109, v109
	v_pk_mul_f32 v[110:111], v[32:33], v[8:9] op_sel_hi:[0,1]
	v_exp_f32_e32 v110, v110
	v_exp_f32_e32 v111, v111
	v_pk_mul_f32 v[112:113], v[126:127], v[116:117] op_sel_hi:[0,1]
	v_pk_fma_f32 v[136:137], v[136:137], v[108:109], v[112:113]
	v_pk_mul_f32 v[108:109], v[126:127], v[118:119] op_sel_hi:[0,1]
	v_pk_fma_f32 v[138:139], v[138:139], v[110:111], v[108:109]
	v_pk_mul_f32 v[108:109], v[32:33], v[2:3] op_sel_hi:[0,1]
	v_exp_f32_e32 v108, v108
	v_exp_f32_e32 v109, v109
	v_pk_mul_f32 v[110:111], v[32:33], v[4:5] op_sel_hi:[0,1]
	v_exp_f32_e32 v110, v110
	v_exp_f32_e32 v111, v111
	v_pk_mul_f32 v[112:113], v[126:127], v[120:121] op_sel_hi:[0,1]
	v_pk_fma_f32 v[124:125], v[124:125], v[108:109], v[112:113]
	v_pk_mul_f32 v[108:109], v[126:127], v[122:123] op_sel_hi:[0,1]
	v_pk_fma_f32 v[104:105], v[104:105], v[110:111], v[108:109]
	s_nop 0
	s_waitcnt lgkmcnt(0)
	s_nop 0
	ds_read_b128 v[108:111], v19 offset:64
	ds_read_b128 v[112:115], v19 offset:80
	ds_read_b128 v[116:119], v19 offset:96
	ds_read_b128 v[120:123], v19 offset:112
	v_mov_b32_e32 v19, 0xa820
	v_pk_mul_f32 v[126:127], v[34:35], v[14:15] op_sel_hi:[0,1]
	v_exp_f32_e32 v126, v126
	v_exp_f32_e32 v127, v127
	v_pk_mul_f32 v[140:141], v[34:35], v[16:17] op_sel_hi:[0,1]
	v_exp_f32_e32 v140, v140
	v_exp_f32_e32 v141, v141
	v_mul_f32_e32 v86, v34, v86
	v_pk_mul_f32 v[88:89], v[86:87], v[88:89] op_sel_hi:[0,1]
	v_pk_fma_f32 v[126:127], v[128:129], v[126:127], v[88:89]
	v_pk_mul_f32 v[88:89], v[86:87], v[90:91] op_sel_hi:[0,1]
	v_pk_fma_f32 v[128:129], v[130:131], v[140:141], v[88:89]
	v_pk_mul_f32 v[88:89], v[34:35], v[10:11] op_sel_hi:[0,1]
	v_exp_f32_e32 v88, v88
	v_exp_f32_e32 v89, v89
	v_pk_mul_f32 v[90:91], v[34:35], v[12:13] op_sel_hi:[0,1]
	v_exp_f32_e32 v90, v90
	v_exp_f32_e32 v91, v91
	v_pk_mul_f32 v[92:93], v[86:87], v[92:93] op_sel_hi:[0,1]
	v_pk_fma_f32 v[130:131], v[132:133], v[88:89], v[92:93]
	v_pk_mul_f32 v[88:89], v[86:87], v[94:95] op_sel_hi:[0,1]
	v_pk_fma_f32 v[132:133], v[134:135], v[90:91], v[88:89]
	v_pk_mul_f32 v[88:89], v[34:35], v[6:7] op_sel_hi:[0,1]
	v_exp_f32_e32 v88, v88
	v_exp_f32_e32 v89, v89
	v_pk_mul_f32 v[90:91], v[34:35], v[8:9] op_sel_hi:[0,1]
	v_exp_f32_e32 v90, v90
	v_exp_f32_e32 v91, v91
	v_pk_mul_f32 v[92:93], v[86:87], v[96:97] op_sel_hi:[0,1]
	v_pk_fma_f32 v[134:135], v[136:137], v[88:89], v[92:93]
	v_pk_mul_f32 v[88:89], v[86:87], v[98:99] op_sel_hi:[0,1]
	v_pk_fma_f32 v[136:137], v[138:139], v[90:91], v[88:89]
	v_pk_mul_f32 v[88:89], v[34:35], v[2:3] op_sel_hi:[0,1]
	v_pk_mul_f32 v[90:91], v[34:35], v[4:5] op_sel_hi:[0,1]
	v_exp_f32_e32 v88, v88
	v_exp_f32_e32 v89, v89
	v_exp_f32_e32 v90, v90
	v_exp_f32_e32 v91, v91
	v_pk_mul_f32 v[92:93], v[86:87], v[100:101] op_sel_hi:[0,1]
	v_pk_mul_f32 v[86:87], v[86:87], v[102:103] op_sel_hi:[0,1]
	v_pk_fma_f32 v[124:125], v[124:125], v[88:89], v[92:93]
	v_pk_fma_f32 v[102:103], v[104:105], v[90:91], v[86:87]
	s_nop 0
	s_waitcnt lgkmcnt(0)
	s_nop 0
	ds_read_b128 v[86:89], v19 offset:64
	ds_read_b128 v[90:93], v19 offset:80
	ds_read_b128 v[94:97], v19 offset:96
	ds_read_b128 v[98:101], v19 offset:112
	v_mov_b32_e32 v19, 0xa8f0
	v_pk_mul_f32 v[138:139], v[36:37], v[14:15] op_sel_hi:[0,1]
	v_exp_f32_e32 v138, v138
	v_exp_f32_e32 v139, v139
	v_pk_mul_f32 v[140:141], v[36:37], v[16:17] op_sel_hi:[0,1]
	v_exp_f32_e32 v140, v140
	v_exp_f32_e32 v141, v141
	v_mul_f32_e32 v104, v36, v85
	v_pk_mul_f32 v[108:109], v[104:105], v[108:109] op_sel_hi:[0,1]
	v_pk_fma_f32 v[126:127], v[126:127], v[138:139], v[108:109]
	v_pk_mul_f32 v[108:109], v[104:105], v[110:111] op_sel_hi:[0,1]
	v_pk_fma_f32 v[128:129], v[128:129], v[140:141], v[108:109]
	v_pk_mul_f32 v[108:109], v[36:37], v[10:11] op_sel_hi:[0,1]
	v_exp_f32_e32 v108, v108
	v_exp_f32_e32 v109, v109
	v_pk_mul_f32 v[110:111], v[36:37], v[12:13] op_sel_hi:[0,1]
	v_exp_f32_e32 v110, v110
	v_exp_f32_e32 v111, v111
	v_pk_mul_f32 v[112:113], v[104:105], v[112:113] op_sel_hi:[0,1]
	v_pk_fma_f32 v[130:131], v[130:131], v[108:109], v[112:113]
	v_pk_mul_f32 v[108:109], v[104:105], v[114:115] op_sel_hi:[0,1]
	v_pk_fma_f32 v[132:133], v[132:133], v[110:111], v[108:109]
	v_pk_mul_f32 v[108:109], v[36:37], v[6:7] op_sel_hi:[0,1]
	v_exp_f32_e32 v108, v108
	v_exp_f32_e32 v109, v109
	v_pk_mul_f32 v[110:111], v[36:37], v[8:9] op_sel_hi:[0,1]
	v_exp_f32_e32 v110, v110
	v_exp_f32_e32 v111, v111
	v_pk_mul_f32 v[112:113], v[104:105], v[116:117] op_sel_hi:[0,1]
	v_pk_fma_f32 v[134:135], v[134:135], v[108:109], v[112:113]
	v_pk_mul_f32 v[108:109], v[104:105], v[118:119] op_sel_hi:[0,1]
	v_pk_fma_f32 v[136:137], v[136:137], v[110:111], v[108:109]
	v_pk_mul_f32 v[108:109], v[36:37], v[2:3] op_sel_hi:[0,1]
	v_pk_mul_f32 v[110:111], v[36:37], v[4:5] op_sel_hi:[0,1]
	v_exp_f32_e32 v108, v108
	v_exp_f32_e32 v109, v109
	v_exp_f32_e32 v110, v110
	v_exp_f32_e32 v111, v111
	v_pk_mul_f32 v[112:113], v[104:105], v[120:121] op_sel_hi:[0,1]
	v_pk_mul_f32 v[104:105], v[104:105], v[122:123] op_sel_hi:[0,1]
	v_pk_fma_f32 v[120:121], v[124:125], v[108:109], v[112:113]
	v_pk_fma_f32 v[122:123], v[102:103], v[110:111], v[104:105]
	s_nop 0
	s_waitcnt lgkmcnt(0)
	s_nop 0
	ds_read_b128 v[102:105], v19 offset:64
	ds_read_b128 v[108:111], v19 offset:80
	ds_read_b128 v[112:115], v19 offset:96
	ds_read_b128 v[116:119], v19 offset:112
	v_mov_b32_e32 v19, 0xa9c0
	v_pk_mul_f32 v[124:125], v[38:39], v[14:15] op_sel_hi:[0,1]
	v_exp_f32_e32 v124, v124
	v_exp_f32_e32 v125, v125
	v_pk_mul_f32 v[138:139], v[38:39], v[16:17] op_sel_hi:[0,1]
	v_exp_f32_e32 v138, v138
	v_exp_f32_e32 v139, v139
	v_mul_f32_e32 v84, v38, v84
	v_pk_mul_f32 v[86:87], v[84:85], v[86:87] op_sel_hi:[0,1]
	v_pk_fma_f32 v[124:125], v[126:127], v[124:125], v[86:87]
	v_pk_mul_f32 v[86:87], v[84:85], v[88:89] op_sel_hi:[0,1]
	v_pk_fma_f32 v[126:127], v[128:129], v[138:139], v[86:87]
	v_pk_mul_f32 v[86:87], v[38:39], v[10:11] op_sel_hi:[0,1]
	v_exp_f32_e32 v86, v86
	v_exp_f32_e32 v87, v87
	v_pk_mul_f32 v[88:89], v[38:39], v[12:13] op_sel_hi:[0,1]
	v_exp_f32_e32 v88, v88
	v_exp_f32_e32 v89, v89
	v_pk_mul_f32 v[90:91], v[84:85], v[90:91] op_sel_hi:[0,1]
	v_pk_fma_f32 v[128:129], v[130:131], v[86:87], v[90:91]
	v_pk_mul_f32 v[86:87], v[84:85], v[92:93] op_sel_hi:[0,1]
	v_pk_fma_f32 v[130:131], v[132:133], v[88:89], v[86:87]
	v_pk_mul_f32 v[86:87], v[38:39], v[6:7] op_sel_hi:[0,1]
	v_exp_f32_e32 v86, v86
	v_exp_f32_e32 v87, v87
	v_pk_mul_f32 v[88:89], v[38:39], v[8:9] op_sel_hi:[0,1]
	v_exp_f32_e32 v88, v88
	v_exp_f32_e32 v89, v89
	v_pk_mul_f32 v[90:91], v[84:85], v[94:95] op_sel_hi:[0,1]
	v_pk_fma_f32 v[132:133], v[134:135], v[86:87], v[90:91]
	v_pk_mul_f32 v[86:87], v[84:85], v[96:97] op_sel_hi:[0,1]
	v_pk_fma_f32 v[134:135], v[136:137], v[88:89], v[86:87]
	v_pk_mul_f32 v[86:87], v[38:39], v[2:3] op_sel_hi:[0,1]
	v_pk_mul_f32 v[88:89], v[38:39], v[4:5] op_sel_hi:[0,1]
	v_exp_f32_e32 v86, v86
	v_exp_f32_e32 v87, v87
	v_exp_f32_e32 v88, v88
	v_exp_f32_e32 v89, v89
	v_pk_mul_f32 v[90:91], v[84:85], v[98:99] op_sel_hi:[0,1]
	v_pk_mul_f32 v[84:85], v[84:85], v[100:101] op_sel_hi:[0,1]
	v_pk_fma_f32 v[120:121], v[120:121], v[86:87], v[90:91]
	v_pk_fma_f32 v[100:101], v[122:123], v[88:89], v[84:85]
	s_nop 0
	s_waitcnt lgkmcnt(0)
	s_nop 0
	ds_read_b128 v[84:87], v19 offset:64
	ds_read_b128 v[88:91], v19 offset:80
	ds_read_b128 v[92:95], v19 offset:96
	ds_read_b128 v[96:99], v19 offset:112
	v_mov_b32_e32 v19, 0xaa90
	v_pk_mul_f32 v[136:137], v[40:41], v[14:15] op_sel_hi:[0,1]
	v_exp_f32_e32 v136, v136
	v_exp_f32_e32 v137, v137
	v_pk_mul_f32 v[138:139], v[40:41], v[16:17] op_sel_hi:[0,1]
	v_exp_f32_e32 v138, v138
	v_exp_f32_e32 v139, v139
	v_mul_f32_e32 v122, v40, v83
	v_pk_mul_f32 v[102:103], v[122:123], v[102:103] op_sel_hi:[0,1]
	v_pk_fma_f32 v[124:125], v[124:125], v[136:137], v[102:103]
	v_pk_mul_f32 v[102:103], v[122:123], v[104:105] op_sel_hi:[0,1]
	v_pk_fma_f32 v[104:105], v[126:127], v[138:139], v[102:103]
	v_pk_mul_f32 v[102:103], v[40:41], v[10:11] op_sel_hi:[0,1]
	v_exp_f32_e32 v102, v102
	v_exp_f32_e32 v103, v103
	v_pk_mul_f32 v[126:127], v[40:41], v[12:13] op_sel_hi:[0,1]
	v_exp_f32_e32 v126, v126
	v_exp_f32_e32 v127, v127
	v_pk_mul_f32 v[108:109], v[122:123], v[108:109] op_sel_hi:[0,1]
	v_pk_fma_f32 v[128:129], v[128:129], v[102:103], v[108:109]
	v_pk_mul_f32 v[102:103], v[122:123], v[110:111] op_sel_hi:[0,1]
	v_pk_fma_f32 v[126:127], v[130:131], v[126:127], v[102:103]
	v_pk_mul_f32 v[102:103], v[40:41], v[6:7] op_sel_hi:[0,1]
	v_exp_f32_e32 v102, v102
	v_exp_f32_e32 v103, v103
	v_pk_mul_f32 v[108:109], v[40:41], v[8:9] op_sel_hi:[0,1]
	v_exp_f32_e32 v108, v108
	v_exp_f32_e32 v109, v109
	v_pk_mul_f32 v[110:111], v[122:123], v[112:113] op_sel_hi:[0,1]
	v_pk_fma_f32 v[130:131], v[132:133], v[102:103], v[110:111]
	v_pk_mul_f32 v[102:103], v[122:123], v[114:115] op_sel_hi:[0,1]
	v_pk_fma_f32 v[132:133], v[134:135], v[108:109], v[102:103]
	v_pk_mul_f32 v[102:103], v[40:41], v[2:3] op_sel_hi:[0,1]
	v_exp_f32_e32 v102, v102
	v_exp_f32_e32 v103, v103
	v_pk_mul_f32 v[108:109], v[40:41], v[4:5] op_sel_hi:[0,1]
	v_exp_f32_e32 v108, v108
	v_exp_f32_e32 v109, v109
	v_pk_mul_f32 v[110:111], v[122:123], v[116:117] op_sel_hi:[0,1]
	v_pk_fma_f32 v[120:121], v[120:121], v[102:103], v[110:111]
	v_pk_mul_f32 v[102:103], v[122:123], v[118:119] op_sel_hi:[0,1]
	v_pk_fma_f32 v[122:123], v[100:101], v[108:109], v[102:103]
	s_nop 0
	s_waitcnt lgkmcnt(0)
	s_nop 0
	ds_read_b128 v[100:103], v19 offset:64
	ds_read_b128 v[108:111], v19 offset:80
	ds_read_b128 v[112:115], v19 offset:96
	ds_read_b128 v[116:119], v19 offset:112
	v_mov_b32_e32 v19, 0xab60
	v_pk_mul_f32 v[134:135], v[42:43], v[14:15] op_sel_hi:[0,1]
	v_exp_f32_e32 v134, v134
	v_exp_f32_e32 v135, v135
	v_pk_mul_f32 v[136:137], v[42:43], v[16:17] op_sel_hi:[0,1]
	v_exp_f32_e32 v136, v136
	v_exp_f32_e32 v137, v137
	v_mul_f32_e32 v82, v42, v82
	v_pk_mul_f32 v[84:85], v[82:83], v[84:85] op_sel_hi:[0,1]
	v_pk_fma_f32 v[124:125], v[124:125], v[134:135], v[84:85]
	v_pk_mul_f32 v[84:85], v[82:83], v[86:87] op_sel_hi:[0,1]
	v_pk_fma_f32 v[104:105], v[104:105], v[136:137], v[84:85]
	v_pk_mul_f32 v[84:85], v[42:43], v[10:11] op_sel_hi:[0,1]
	v_exp_f32_e32 v84, v84
	v_exp_f32_e32 v85, v85
	v_pk_mul_f32 v[86:87], v[42:43], v[12:13] op_sel_hi:[0,1]
	v_exp_f32_e32 v86, v86
	v_exp_f32_e32 v87, v87
	v_pk_mul_f32 v[88:89], v[82:83], v[88:89] op_sel_hi:[0,1]
	v_pk_fma_f32 v[128:129], v[128:129], v[84:85], v[88:89]
	v_pk_mul_f32 v[84:85], v[82:83], v[90:91] op_sel_hi:[0,1]
	v_pk_fma_f32 v[126:127], v[126:127], v[86:87], v[84:85]
	v_pk_mul_f32 v[84:85], v[42:43], v[6:7] op_sel_hi:[0,1]
	v_exp_f32_e32 v84, v84
	v_exp_f32_e32 v85, v85
	v_pk_mul_f32 v[86:87], v[42:43], v[8:9] op_sel_hi:[0,1]
	v_exp_f32_e32 v86, v86
	v_exp_f32_e32 v87, v87
	v_pk_mul_f32 v[88:89], v[82:83], v[92:93] op_sel_hi:[0,1]
	v_pk_fma_f32 v[130:131], v[130:131], v[84:85], v[88:89]
	v_pk_mul_f32 v[84:85], v[82:83], v[94:95] op_sel_hi:[0,1]
	v_pk_fma_f32 v[132:133], v[132:133], v[86:87], v[84:85]
	v_pk_mul_f32 v[84:85], v[42:43], v[2:3] op_sel_hi:[0,1]
	v_pk_mul_f32 v[86:87], v[42:43], v[4:5] op_sel_hi:[0,1]
	v_exp_f32_e32 v84, v84
	v_exp_f32_e32 v85, v85
	v_exp_f32_e32 v86, v86
	v_exp_f32_e32 v87, v87
	v_pk_mul_f32 v[88:89], v[82:83], v[96:97] op_sel_hi:[0,1]
	v_pk_mul_f32 v[82:83], v[82:83], v[98:99] op_sel_hi:[0,1]
	v_pk_fma_f32 v[120:121], v[120:121], v[84:85], v[88:89]
	v_pk_fma_f32 v[98:99], v[122:123], v[86:87], v[82:83]
	s_nop 0
	s_waitcnt lgkmcnt(0)
	s_nop 0
	ds_read_b128 v[82:85], v19 offset:64
	ds_read_b128 v[86:89], v19 offset:80
	ds_read_b128 v[90:93], v19 offset:96
	ds_read_b128 v[94:97], v19 offset:112
	v_mov_b32_e32 v19, 0xac30
	v_pk_mul_f32 v[134:135], v[44:45], v[14:15] op_sel_hi:[0,1]
	v_exp_f32_e32 v134, v134
	v_exp_f32_e32 v135, v135
	v_pk_mul_f32 v[136:137], v[44:45], v[16:17] op_sel_hi:[0,1]
	v_exp_f32_e32 v136, v136
	v_exp_f32_e32 v137, v137
	v_mul_f32_e32 v122, v44, v81
	v_pk_mul_f32 v[100:101], v[122:123], v[100:101] op_sel_hi:[0,1]
	v_pk_fma_f32 v[124:125], v[124:125], v[134:135], v[100:101]
	v_pk_mul_f32 v[100:101], v[122:123], v[102:103] op_sel_hi:[0,1]
	v_pk_fma_f32 v[134:135], v[104:105], v[136:137], v[100:101]
	v_pk_mul_f32 v[100:101], v[44:45], v[10:11] op_sel_hi:[0,1]
	v_exp_f32_e32 v100, v100
	v_exp_f32_e32 v101, v101
	v_pk_mul_f32 v[102:103], v[44:45], v[12:13] op_sel_hi:[0,1]
	v_exp_f32_e32 v102, v102
	v_exp_f32_e32 v103, v103
	v_pk_mul_f32 v[104:105], v[122:123], v[108:109] op_sel_hi:[0,1]
	v_pk_fma_f32 v[128:129], v[128:129], v[100:101], v[104:105]
	v_pk_mul_f32 v[100:101], v[122:123], v[110:111] op_sel_hi:[0,1]
	v_pk_fma_f32 v[126:127], v[126:127], v[102:103], v[100:101]
	v_pk_mul_f32 v[100:101], v[44:45], v[6:7] op_sel_hi:[0,1]
	v_exp_f32_e32 v100, v100
	v_exp_f32_e32 v101, v101
	v_pk_mul_f32 v[102:103], v[44:45], v[8:9] op_sel_hi:[0,1]
	v_exp_f32_e32 v102, v102
	v_exp_f32_e32 v103, v103
	v_pk_mul_f32 v[104:105], v[122:123], v[112:113] op_sel_hi:[0,1]
	v_pk_fma_f32 v[130:131], v[130:131], v[100:101], v[104:105]
	v_pk_mul_f32 v[100:101], v[122:123], v[114:115] op_sel_hi:[0,1]
	v_pk_fma_f32 v[132:133], v[132:133], v[102:103], v[100:101]
	v_pk_mul_f32 v[100:101], v[44:45], v[2:3] op_sel_hi:[0,1]
	v_exp_f32_e32 v100, v100
	v_exp_f32_e32 v101, v101
	v_pk_mul_f32 v[102:103], v[44:45], v[4:5] op_sel_hi:[0,1]
	v_exp_f32_e32 v102, v102
	v_exp_f32_e32 v103, v103
	v_pk_mul_f32 v[104:105], v[122:123], v[116:117] op_sel_hi:[0,1]
	v_pk_fma_f32 v[116:117], v[120:121], v[100:101], v[104:105]
	v_pk_mul_f32 v[100:101], v[122:123], v[118:119] op_sel_hi:[0,1]
	v_pk_fma_f32 v[118:119], v[98:99], v[102:103], v[100:101]
	s_nop 0
	s_waitcnt lgkmcnt(0)
	s_nop 0
	ds_read_b128 v[98:101], v19 offset:64
	ds_read_b128 v[102:105], v19 offset:80
	ds_read_b128 v[108:111], v19 offset:96
	ds_read_b128 v[112:115], v19 offset:112
	v_mov_b32_e32 v19, 0xad00
	v_pk_mul_f32 v[122:123], v[46:47], v[14:15] op_sel_hi:[0,1]
	v_exp_f32_e32 v122, v122
	v_exp_f32_e32 v123, v123
	v_pk_mul_f32 v[136:137], v[46:47], v[16:17] op_sel_hi:[0,1]
	v_exp_f32_e32 v136, v136
	v_exp_f32_e32 v137, v137
	v_mul_f32_e32 v120, v46, v79
	v_pk_mul_f32 v[82:83], v[120:121], v[82:83] op_sel_hi:[0,1]
	v_pk_fma_f32 v[122:123], v[124:125], v[122:123], v[82:83]
	v_pk_mul_f32 v[82:83], v[120:121], v[84:85] op_sel_hi:[0,1]
	v_pk_fma_f32 v[124:125], v[134:135], v[136:137], v[82:83]
	v_pk_mul_f32 v[82:83], v[46:47], v[10:11] op_sel_hi:[0,1]
	v_exp_f32_e32 v82, v82
	v_exp_f32_e32 v83, v83
	v_pk_mul_f32 v[84:85], v[46:47], v[12:13] op_sel_hi:[0,1]
	v_exp_f32_e32 v84, v84
	v_exp_f32_e32 v85, v85
	v_pk_mul_f32 v[86:87], v[120:121], v[86:87] op_sel_hi:[0,1]
	v_pk_fma_f32 v[128:129], v[128:129], v[82:83], v[86:87]
	v_pk_mul_f32 v[82:83], v[120:121], v[88:89] op_sel_hi:[0,1]
	v_pk_fma_f32 v[126:127], v[126:127], v[84:85], v[82:83]
	v_pk_mul_f32 v[82:83], v[46:47], v[6:7] op_sel_hi:[0,1]
	v_exp_f32_e32 v82, v82
	v_exp_f32_e32 v83, v83
	v_pk_mul_f32 v[84:85], v[46:47], v[8:9] op_sel_hi:[0,1]
	v_exp_f32_e32 v84, v84
	v_exp_f32_e32 v85, v85
	v_pk_mul_f32 v[86:87], v[120:121], v[90:91] op_sel_hi:[0,1]
	v_pk_fma_f32 v[130:131], v[130:131], v[82:83], v[86:87]
	v_pk_mul_f32 v[82:83], v[120:121], v[92:93] op_sel_hi:[0,1]
	v_pk_fma_f32 v[132:133], v[132:133], v[84:85], v[82:83]
	v_pk_mul_f32 v[82:83], v[46:47], v[2:3] op_sel_hi:[0,1]
	v_exp_f32_e32 v82, v82
	v_exp_f32_e32 v83, v83
	v_pk_mul_f32 v[84:85], v[46:47], v[4:5] op_sel_hi:[0,1]
	v_exp_f32_e32 v84, v84
	v_exp_f32_e32 v85, v85
	v_pk_mul_f32 v[86:87], v[120:121], v[94:95] op_sel_hi:[0,1]
	v_pk_fma_f32 v[116:117], v[116:117], v[82:83], v[86:87]
	v_pk_mul_f32 v[82:83], v[120:121], v[96:97] op_sel_hi:[0,1]
	v_pk_fma_f32 v[118:119], v[118:119], v[84:85], v[82:83]
	s_nop 0
	s_waitcnt lgkmcnt(0)
	s_nop 0
	ds_read_b128 v[82:85], v19 offset:64
	ds_read_b128 v[86:89], v19 offset:80
	ds_read_b128 v[90:93], v19 offset:96
	ds_read_b128 v[94:97], v19 offset:112
	v_mov_b32_e32 v19, 0xadd0
	v_pk_mul_f32 v[134:135], v[48:49], v[14:15] op_sel_hi:[0,1]
	v_exp_f32_e32 v134, v134
	v_exp_f32_e32 v135, v135
	v_pk_mul_f32 v[136:137], v[48:49], v[16:17] op_sel_hi:[0,1]
	v_exp_f32_e32 v136, v136
	v_exp_f32_e32 v137, v137
	v_mul_f32_e32 v120, v48, v77
	v_pk_mul_f32 v[98:99], v[120:121], v[98:99] op_sel_hi:[0,1]
	v_pk_fma_f32 v[122:123], v[122:123], v[134:135], v[98:99]
	v_pk_mul_f32 v[98:99], v[120:121], v[100:101] op_sel_hi:[0,1]
	v_pk_fma_f32 v[124:125], v[124:125], v[136:137], v[98:99]
	v_pk_mul_f32 v[98:99], v[48:49], v[10:11] op_sel_hi:[0,1]
	v_exp_f32_e32 v98, v98
	v_exp_f32_e32 v99, v99
	v_pk_mul_f32 v[100:101], v[48:49], v[12:13] op_sel_hi:[0,1]
	v_exp_f32_e32 v100, v100
	v_exp_f32_e32 v101, v101
	v_pk_mul_f32 v[102:103], v[120:121], v[102:103] op_sel_hi:[0,1]
	v_pk_fma_f32 v[128:129], v[128:129], v[98:99], v[102:103]
	v_pk_mul_f32 v[98:99], v[120:121], v[104:105] op_sel_hi:[0,1]
	v_pk_fma_f32 v[126:127], v[126:127], v[100:101], v[98:99]
	v_pk_mul_f32 v[98:99], v[48:49], v[6:7] op_sel_hi:[0,1]
	v_exp_f32_e32 v98, v98
	v_exp_f32_e32 v99, v99
	v_pk_mul_f32 v[100:101], v[48:49], v[8:9] op_sel_hi:[0,1]
	v_exp_f32_e32 v100, v100
	v_exp_f32_e32 v101, v101
	v_pk_mul_f32 v[102:103], v[120:121], v[108:109] op_sel_hi:[0,1]
	v_pk_fma_f32 v[130:131], v[130:131], v[98:99], v[102:103]
	v_pk_mul_f32 v[98:99], v[120:121], v[110:111] op_sel_hi:[0,1]
	v_pk_fma_f32 v[132:133], v[132:133], v[100:101], v[98:99]
	v_pk_mul_f32 v[98:99], v[48:49], v[2:3] op_sel_hi:[0,1]
	v_exp_f32_e32 v98, v98
	v_exp_f32_e32 v99, v99
	v_pk_mul_f32 v[100:101], v[48:49], v[4:5] op_sel_hi:[0,1]
	v_exp_f32_e32 v100, v100
	v_exp_f32_e32 v101, v101
	v_pk_mul_f32 v[102:103], v[120:121], v[112:113] op_sel_hi:[0,1]
	v_pk_fma_f32 v[116:117], v[116:117], v[98:99], v[102:103]
	v_pk_mul_f32 v[98:99], v[120:121], v[114:115] op_sel_hi:[0,1]
	v_pk_fma_f32 v[118:119], v[118:119], v[100:101], v[98:99]
	s_nop 0
	s_waitcnt lgkmcnt(0)
	s_nop 0
	ds_read_b128 v[98:101], v19 offset:64
	ds_read_b128 v[102:105], v19 offset:80
	ds_read_b128 v[108:111], v19 offset:96
	ds_read_b128 v[112:115], v19 offset:112
	v_mov_b32_e32 v19, 0xaea0
	v_pk_mul_f32 v[134:135], v[50:51], v[14:15] op_sel_hi:[0,1]
	v_exp_f32_e32 v134, v134
	v_exp_f32_e32 v135, v135
	v_pk_mul_f32 v[136:137], v[50:51], v[16:17] op_sel_hi:[0,1]
	v_exp_f32_e32 v136, v136
	v_exp_f32_e32 v137, v137
	v_mul_f32_e32 v120, v50, v75
	v_pk_mul_f32 v[82:83], v[120:121], v[82:83] op_sel_hi:[0,1]
	v_pk_fma_f32 v[122:123], v[122:123], v[134:135], v[82:83]
	v_pk_mul_f32 v[82:83], v[120:121], v[84:85] op_sel_hi:[0,1]
	v_pk_fma_f32 v[124:125], v[124:125], v[136:137], v[82:83]
	v_pk_mul_f32 v[82:83], v[50:51], v[10:11] op_sel_hi:[0,1]
	v_exp_f32_e32 v82, v82
	v_exp_f32_e32 v83, v83
	v_pk_mul_f32 v[84:85], v[50:51], v[12:13] op_sel_hi:[0,1]
	v_exp_f32_e32 v84, v84
	v_exp_f32_e32 v85, v85
	v_pk_mul_f32 v[86:87], v[120:121], v[86:87] op_sel_hi:[0,1]
	v_pk_fma_f32 v[128:129], v[128:129], v[82:83], v[86:87]
	v_pk_mul_f32 v[82:83], v[120:121], v[88:89] op_sel_hi:[0,1]
	v_pk_fma_f32 v[126:127], v[126:127], v[84:85], v[82:83]
	v_pk_mul_f32 v[82:83], v[50:51], v[6:7] op_sel_hi:[0,1]
	v_exp_f32_e32 v82, v82
	v_exp_f32_e32 v83, v83
	v_pk_mul_f32 v[84:85], v[50:51], v[8:9] op_sel_hi:[0,1]
	v_exp_f32_e32 v84, v84
	v_exp_f32_e32 v85, v85
	v_pk_mul_f32 v[86:87], v[120:121], v[90:91] op_sel_hi:[0,1]
	v_pk_fma_f32 v[130:131], v[130:131], v[82:83], v[86:87]
	v_pk_mul_f32 v[82:83], v[120:121], v[92:93] op_sel_hi:[0,1]
	v_pk_fma_f32 v[132:133], v[132:133], v[84:85], v[82:83]
	v_pk_mul_f32 v[82:83], v[50:51], v[2:3] op_sel_hi:[0,1]
	v_exp_f32_e32 v82, v82
	v_exp_f32_e32 v83, v83
	v_pk_mul_f32 v[84:85], v[50:51], v[4:5] op_sel_hi:[0,1]
	v_exp_f32_e32 v84, v84
	v_exp_f32_e32 v85, v85
	v_pk_mul_f32 v[86:87], v[120:121], v[94:95] op_sel_hi:[0,1]
	v_pk_fma_f32 v[116:117], v[116:117], v[82:83], v[86:87]
	v_pk_mul_f32 v[82:83], v[120:121], v[96:97] op_sel_hi:[0,1]
	v_pk_fma_f32 v[118:119], v[118:119], v[84:85], v[82:83]
	s_nop 0
	s_waitcnt lgkmcnt(0)
	s_nop 0
	ds_read_b128 v[82:85], v19 offset:64
	ds_read_b128 v[86:89], v19 offset:80
	ds_read_b128 v[90:93], v19 offset:96
	ds_read_b128 v[94:97], v19 offset:112
	v_mov_b32_e32 v19, 0xaf70
	v_pk_mul_f32 v[134:135], v[52:53], v[14:15] op_sel_hi:[0,1]
	v_exp_f32_e32 v134, v134
	v_exp_f32_e32 v135, v135
	v_pk_mul_f32 v[136:137], v[52:53], v[16:17] op_sel_hi:[0,1]
	v_exp_f32_e32 v136, v136
	v_exp_f32_e32 v137, v137
	v_mul_f32_e32 v120, v52, v73
	v_pk_mul_f32 v[98:99], v[120:121], v[98:99] op_sel_hi:[0,1]
	v_pk_fma_f32 v[122:123], v[122:123], v[134:135], v[98:99]
	v_pk_mul_f32 v[98:99], v[120:121], v[100:101] op_sel_hi:[0,1]
	v_pk_fma_f32 v[124:125], v[124:125], v[136:137], v[98:99]
	v_pk_mul_f32 v[98:99], v[52:53], v[10:11] op_sel_hi:[0,1]
	v_exp_f32_e32 v98, v98
	v_exp_f32_e32 v99, v99
	v_pk_mul_f32 v[100:101], v[52:53], v[12:13] op_sel_hi:[0,1]
	v_exp_f32_e32 v100, v100
	v_exp_f32_e32 v101, v101
	v_pk_mul_f32 v[102:103], v[120:121], v[102:103] op_sel_hi:[0,1]
	v_pk_fma_f32 v[128:129], v[128:129], v[98:99], v[102:103]
	v_pk_mul_f32 v[98:99], v[120:121], v[104:105] op_sel_hi:[0,1]
	v_pk_fma_f32 v[126:127], v[126:127], v[100:101], v[98:99]
	v_pk_mul_f32 v[98:99], v[52:53], v[6:7] op_sel_hi:[0,1]
	v_exp_f32_e32 v98, v98
	v_exp_f32_e32 v99, v99
	v_pk_mul_f32 v[100:101], v[52:53], v[8:9] op_sel_hi:[0,1]
	v_exp_f32_e32 v100, v100
	v_exp_f32_e32 v101, v101
	v_pk_mul_f32 v[102:103], v[120:121], v[108:109] op_sel_hi:[0,1]
	v_pk_fma_f32 v[130:131], v[130:131], v[98:99], v[102:103]
	v_pk_mul_f32 v[98:99], v[120:121], v[110:111] op_sel_hi:[0,1]
	v_pk_fma_f32 v[132:133], v[132:133], v[100:101], v[98:99]
	v_pk_mul_f32 v[98:99], v[52:53], v[2:3] op_sel_hi:[0,1]
	v_exp_f32_e32 v98, v98
	v_exp_f32_e32 v99, v99
	v_pk_mul_f32 v[100:101], v[52:53], v[4:5] op_sel_hi:[0,1]
	v_exp_f32_e32 v100, v100
	v_exp_f32_e32 v101, v101
	v_pk_mul_f32 v[102:103], v[120:121], v[112:113] op_sel_hi:[0,1]
	v_pk_fma_f32 v[116:117], v[116:117], v[98:99], v[102:103]
	v_pk_mul_f32 v[98:99], v[120:121], v[114:115] op_sel_hi:[0,1]
	v_pk_fma_f32 v[118:119], v[118:119], v[100:101], v[98:99]
	s_nop 0
	s_waitcnt lgkmcnt(0)
	s_nop 0
	ds_read_b128 v[98:101], v19 offset:64
	ds_read_b128 v[102:105], v19 offset:80
	ds_read_b128 v[108:111], v19 offset:96
	ds_read_b128 v[112:115], v19 offset:112
	v_mov_b32_e32 v19, 0xb040
	v_pk_mul_f32 v[134:135], v[54:55], v[14:15] op_sel_hi:[0,1]
	v_exp_f32_e32 v134, v134
	v_exp_f32_e32 v135, v135
	v_pk_mul_f32 v[136:137], v[54:55], v[16:17] op_sel_hi:[0,1]
	v_exp_f32_e32 v136, v136
	v_exp_f32_e32 v137, v137
	v_mul_f32_e32 v120, v54, v71
	v_pk_mul_f32 v[82:83], v[120:121], v[82:83] op_sel_hi:[0,1]
	v_pk_fma_f32 v[122:123], v[122:123], v[134:135], v[82:83]
	v_pk_mul_f32 v[82:83], v[120:121], v[84:85] op_sel_hi:[0,1]
	v_pk_fma_f32 v[124:125], v[124:125], v[136:137], v[82:83]
	v_pk_mul_f32 v[82:83], v[54:55], v[10:11] op_sel_hi:[0,1]
	v_exp_f32_e32 v82, v82
	v_exp_f32_e32 v83, v83
	v_pk_mul_f32 v[84:85], v[54:55], v[12:13] op_sel_hi:[0,1]
	v_exp_f32_e32 v84, v84
	v_exp_f32_e32 v85, v85
	v_pk_mul_f32 v[86:87], v[120:121], v[86:87] op_sel_hi:[0,1]
	v_pk_fma_f32 v[128:129], v[128:129], v[82:83], v[86:87]
	v_pk_mul_f32 v[82:83], v[120:121], v[88:89] op_sel_hi:[0,1]
	v_pk_fma_f32 v[126:127], v[126:127], v[84:85], v[82:83]
	v_pk_mul_f32 v[82:83], v[54:55], v[6:7] op_sel_hi:[0,1]
	v_exp_f32_e32 v82, v82
	v_exp_f32_e32 v83, v83
	v_pk_mul_f32 v[84:85], v[54:55], v[8:9] op_sel_hi:[0,1]
	v_exp_f32_e32 v84, v84
	v_exp_f32_e32 v85, v85
	v_pk_mul_f32 v[86:87], v[120:121], v[90:91] op_sel_hi:[0,1]
	v_pk_fma_f32 v[130:131], v[130:131], v[82:83], v[86:87]
	v_pk_mul_f32 v[82:83], v[120:121], v[92:93] op_sel_hi:[0,1]
	v_pk_fma_f32 v[132:133], v[132:133], v[84:85], v[82:83]
	v_pk_mul_f32 v[82:83], v[54:55], v[2:3] op_sel_hi:[0,1]
	v_exp_f32_e32 v82, v82
	v_exp_f32_e32 v83, v83
	v_pk_mul_f32 v[84:85], v[54:55], v[4:5] op_sel_hi:[0,1]
	v_exp_f32_e32 v84, v84
	v_exp_f32_e32 v85, v85
	v_pk_mul_f32 v[86:87], v[120:121], v[94:95] op_sel_hi:[0,1]
	v_pk_fma_f32 v[116:117], v[116:117], v[82:83], v[86:87]
	v_pk_mul_f32 v[82:83], v[120:121], v[96:97] op_sel_hi:[0,1]
	v_pk_fma_f32 v[118:119], v[118:119], v[84:85], v[82:83]
	s_nop 0
	s_waitcnt lgkmcnt(0)
	s_nop 0
	ds_read_b128 v[82:85], v19 offset:64
	ds_read_b128 v[86:89], v19 offset:80
	ds_read_b128 v[90:93], v19 offset:96
	ds_read_b128 v[94:97], v19 offset:112
	v_mov_b32_e32 v19, 0xb110
	v_pk_mul_f32 v[134:135], v[56:57], v[14:15] op_sel_hi:[0,1]
	v_exp_f32_e32 v134, v134
	v_exp_f32_e32 v135, v135
	v_pk_mul_f32 v[136:137], v[56:57], v[16:17] op_sel_hi:[0,1]
	v_exp_f32_e32 v136, v136
	v_exp_f32_e32 v137, v137
	v_mul_f32_e32 v120, v56, v69
	v_pk_mul_f32 v[98:99], v[120:121], v[98:99] op_sel_hi:[0,1]
	v_pk_fma_f32 v[122:123], v[122:123], v[134:135], v[98:99]
	v_pk_mul_f32 v[98:99], v[120:121], v[100:101] op_sel_hi:[0,1]
	v_pk_fma_f32 v[124:125], v[124:125], v[136:137], v[98:99]
	v_pk_mul_f32 v[98:99], v[56:57], v[10:11] op_sel_hi:[0,1]
	v_exp_f32_e32 v98, v98
	v_exp_f32_e32 v99, v99
	v_pk_mul_f32 v[100:101], v[56:57], v[12:13] op_sel_hi:[0,1]
	v_exp_f32_e32 v100, v100
	v_exp_f32_e32 v101, v101
	v_pk_mul_f32 v[102:103], v[120:121], v[102:103] op_sel_hi:[0,1]
	v_pk_fma_f32 v[128:129], v[128:129], v[98:99], v[102:103]
	v_pk_mul_f32 v[98:99], v[120:121], v[104:105] op_sel_hi:[0,1]
	v_pk_fma_f32 v[126:127], v[126:127], v[100:101], v[98:99]
	v_pk_mul_f32 v[98:99], v[56:57], v[6:7] op_sel_hi:[0,1]
	v_exp_f32_e32 v98, v98
	v_exp_f32_e32 v99, v99
	v_pk_mul_f32 v[100:101], v[56:57], v[8:9] op_sel_hi:[0,1]
	v_exp_f32_e32 v100, v100
	v_exp_f32_e32 v101, v101
	v_pk_mul_f32 v[102:103], v[120:121], v[108:109] op_sel_hi:[0,1]
	v_pk_fma_f32 v[130:131], v[130:131], v[98:99], v[102:103]
	v_pk_mul_f32 v[98:99], v[120:121], v[110:111] op_sel_hi:[0,1]
	v_pk_fma_f32 v[132:133], v[132:133], v[100:101], v[98:99]
	v_pk_mul_f32 v[98:99], v[56:57], v[2:3] op_sel_hi:[0,1]
	v_exp_f32_e32 v98, v98
	v_exp_f32_e32 v99, v99
	v_pk_mul_f32 v[100:101], v[56:57], v[4:5] op_sel_hi:[0,1]
	v_exp_f32_e32 v100, v100
	v_exp_f32_e32 v101, v101
	v_pk_mul_f32 v[102:103], v[120:121], v[112:113] op_sel_hi:[0,1]
	v_pk_fma_f32 v[116:117], v[116:117], v[98:99], v[102:103]
	v_pk_mul_f32 v[98:99], v[120:121], v[114:115] op_sel_hi:[0,1]
	v_pk_fma_f32 v[118:119], v[118:119], v[100:101], v[98:99]
	s_nop 0
	s_waitcnt lgkmcnt(0)
	s_nop 0
	ds_read_b128 v[98:101], v19 offset:64
	ds_read_b128 v[102:105], v19 offset:80
	ds_read_b128 v[108:111], v19 offset:96
	ds_read_b128 v[112:115], v19 offset:112
	v_mov_b32_e32 v19, 0xb1e0
	v_pk_mul_f32 v[134:135], v[58:59], v[14:15] op_sel_hi:[0,1]
	v_exp_f32_e32 v134, v134
	v_exp_f32_e32 v135, v135
	v_pk_mul_f32 v[136:137], v[58:59], v[16:17] op_sel_hi:[0,1]
	v_exp_f32_e32 v136, v136
	v_exp_f32_e32 v137, v137
	v_mul_f32_e32 v120, v58, v67
	v_pk_mul_f32 v[82:83], v[120:121], v[82:83] op_sel_hi:[0,1]
	v_pk_fma_f32 v[122:123], v[122:123], v[134:135], v[82:83]
	v_pk_mul_f32 v[82:83], v[120:121], v[84:85] op_sel_hi:[0,1]
	v_pk_fma_f32 v[124:125], v[124:125], v[136:137], v[82:83]
	v_pk_mul_f32 v[82:83], v[58:59], v[10:11] op_sel_hi:[0,1]
	v_exp_f32_e32 v82, v82
	v_exp_f32_e32 v83, v83
	v_pk_mul_f32 v[84:85], v[58:59], v[12:13] op_sel_hi:[0,1]
	v_exp_f32_e32 v84, v84
	v_exp_f32_e32 v85, v85
	v_pk_mul_f32 v[86:87], v[120:121], v[86:87] op_sel_hi:[0,1]
	v_pk_fma_f32 v[128:129], v[128:129], v[82:83], v[86:87]
	v_pk_mul_f32 v[82:83], v[120:121], v[88:89] op_sel_hi:[0,1]
	v_pk_fma_f32 v[126:127], v[126:127], v[84:85], v[82:83]
	v_pk_mul_f32 v[82:83], v[58:59], v[6:7] op_sel_hi:[0,1]
	v_exp_f32_e32 v82, v82
	v_exp_f32_e32 v83, v83
	v_pk_mul_f32 v[84:85], v[58:59], v[8:9] op_sel_hi:[0,1]
	v_exp_f32_e32 v84, v84
	v_exp_f32_e32 v85, v85
	v_pk_mul_f32 v[86:87], v[120:121], v[90:91] op_sel_hi:[0,1]
	v_pk_fma_f32 v[130:131], v[130:131], v[82:83], v[86:87]
	v_pk_mul_f32 v[82:83], v[120:121], v[92:93] op_sel_hi:[0,1]
	v_pk_fma_f32 v[132:133], v[132:133], v[84:85], v[82:83]
	v_pk_mul_f32 v[82:83], v[58:59], v[2:3] op_sel_hi:[0,1]
	v_exp_f32_e32 v82, v82
	v_exp_f32_e32 v83, v83
	v_pk_mul_f32 v[84:85], v[58:59], v[4:5] op_sel_hi:[0,1]
	v_exp_f32_e32 v84, v84
	v_exp_f32_e32 v85, v85
	v_pk_mul_f32 v[86:87], v[120:121], v[94:95] op_sel_hi:[0,1]
	v_pk_fma_f32 v[116:117], v[116:117], v[82:83], v[86:87]
	v_pk_mul_f32 v[82:83], v[120:121], v[96:97] op_sel_hi:[0,1]
	v_pk_fma_f32 v[118:119], v[118:119], v[84:85], v[82:83]
	s_nop 0
	s_waitcnt lgkmcnt(0)
	s_nop 0
	ds_read_b128 v[82:85], v19 offset:64
	ds_read_b128 v[86:89], v19 offset:80
	ds_read_b128 v[90:93], v19 offset:96
	ds_read_b128 v[94:97], v19 offset:112
	v_mov_b32_e32 v19, 0xb2b0
	v_pk_mul_f32 v[134:135], v[60:61], v[14:15] op_sel_hi:[0,1]
	v_exp_f32_e32 v134, v134
	v_exp_f32_e32 v135, v135
	v_pk_mul_f32 v[136:137], v[60:61], v[16:17] op_sel_hi:[0,1]
	v_exp_f32_e32 v136, v136
	v_exp_f32_e32 v137, v137
	v_mul_f32_e32 v120, v60, v65
	v_pk_mul_f32 v[98:99], v[120:121], v[98:99] op_sel_hi:[0,1]
	v_pk_fma_f32 v[122:123], v[122:123], v[134:135], v[98:99]
	v_pk_mul_f32 v[98:99], v[120:121], v[100:101] op_sel_hi:[0,1]
	v_pk_fma_f32 v[124:125], v[124:125], v[136:137], v[98:99]
	v_pk_mul_f32 v[98:99], v[60:61], v[10:11] op_sel_hi:[0,1]
	v_exp_f32_e32 v98, v98
	v_exp_f32_e32 v99, v99
	v_pk_mul_f32 v[100:101], v[60:61], v[12:13] op_sel_hi:[0,1]
	v_exp_f32_e32 v100, v100
	v_exp_f32_e32 v101, v101
	v_pk_mul_f32 v[102:103], v[120:121], v[102:103] op_sel_hi:[0,1]
	v_pk_fma_f32 v[128:129], v[128:129], v[98:99], v[102:103]
	v_pk_mul_f32 v[98:99], v[120:121], v[104:105] op_sel_hi:[0,1]
	v_pk_fma_f32 v[126:127], v[126:127], v[100:101], v[98:99]
	v_pk_mul_f32 v[98:99], v[60:61], v[6:7] op_sel_hi:[0,1]
	v_exp_f32_e32 v98, v98
	v_exp_f32_e32 v99, v99
	v_pk_mul_f32 v[100:101], v[60:61], v[8:9] op_sel_hi:[0,1]
	v_exp_f32_e32 v100, v100
	v_exp_f32_e32 v101, v101
	v_pk_mul_f32 v[102:103], v[120:121], v[108:109] op_sel_hi:[0,1]
	v_pk_fma_f32 v[130:131], v[130:131], v[98:99], v[102:103]
	v_pk_mul_f32 v[98:99], v[120:121], v[110:111] op_sel_hi:[0,1]
	v_pk_fma_f32 v[132:133], v[132:133], v[100:101], v[98:99]
	v_pk_mul_f32 v[98:99], v[60:61], v[2:3] op_sel_hi:[0,1]
	v_exp_f32_e32 v98, v98
	v_exp_f32_e32 v99, v99
	v_pk_mul_f32 v[100:101], v[60:61], v[4:5] op_sel_hi:[0,1]
	v_exp_f32_e32 v100, v100
	v_exp_f32_e32 v101, v101
	v_pk_mul_f32 v[102:103], v[120:121], v[112:113] op_sel_hi:[0,1]
	v_pk_fma_f32 v[116:117], v[116:117], v[98:99], v[102:103]
	v_pk_mul_f32 v[98:99], v[120:121], v[114:115] op_sel_hi:[0,1]
	v_pk_fma_f32 v[118:119], v[118:119], v[100:101], v[98:99]
	s_nop 0
	s_waitcnt lgkmcnt(0)
	s_nop 0
	ds_read_b128 v[98:101], v19 offset:64
	ds_read_b128 v[102:105], v19 offset:80
	ds_read_b128 v[108:111], v19 offset:96
	ds_read_b128 v[112:115], v19 offset:112
	v_mov_b32_e32 v19, 0xb380
	v_pk_mul_f32 v[134:135], v[62:63], v[14:15] op_sel_hi:[0,1]
	v_exp_f32_e32 v134, v134
	v_exp_f32_e32 v135, v135
	v_pk_mul_f32 v[136:137], v[62:63], v[16:17] op_sel_hi:[0,1]
	v_exp_f32_e32 v136, v136
	v_exp_f32_e32 v137, v137
	v_mul_f32_e32 v120, v62, v63
	v_pk_mul_f32 v[82:83], v[120:121], v[82:83] op_sel_hi:[0,1]
	v_pk_fma_f32 v[122:123], v[122:123], v[134:135], v[82:83]
	v_pk_mul_f32 v[82:83], v[120:121], v[84:85] op_sel_hi:[0,1]
	v_pk_fma_f32 v[124:125], v[124:125], v[136:137], v[82:83]
	v_pk_mul_f32 v[82:83], v[62:63], v[10:11] op_sel_hi:[0,1]
	v_exp_f32_e32 v82, v82
	v_exp_f32_e32 v83, v83
	v_pk_mul_f32 v[84:85], v[62:63], v[12:13] op_sel_hi:[0,1]
	v_exp_f32_e32 v84, v84
	v_exp_f32_e32 v85, v85
	v_pk_mul_f32 v[86:87], v[120:121], v[86:87] op_sel_hi:[0,1]
	v_pk_fma_f32 v[128:129], v[128:129], v[82:83], v[86:87]
	v_pk_mul_f32 v[82:83], v[120:121], v[88:89] op_sel_hi:[0,1]
	v_pk_fma_f32 v[126:127], v[126:127], v[84:85], v[82:83]
	v_pk_mul_f32 v[82:83], v[62:63], v[6:7] op_sel_hi:[0,1]
	v_exp_f32_e32 v82, v82
	v_exp_f32_e32 v83, v83
	v_pk_mul_f32 v[84:85], v[62:63], v[8:9] op_sel_hi:[0,1]
	v_exp_f32_e32 v84, v84
	v_exp_f32_e32 v85, v85
	v_pk_mul_f32 v[86:87], v[120:121], v[90:91] op_sel_hi:[0,1]
	v_pk_fma_f32 v[130:131], v[130:131], v[82:83], v[86:87]
	v_pk_mul_f32 v[82:83], v[120:121], v[92:93] op_sel_hi:[0,1]
	v_pk_fma_f32 v[132:133], v[132:133], v[84:85], v[82:83]
	v_pk_mul_f32 v[82:83], v[62:63], v[2:3] op_sel_hi:[0,1]
	v_exp_f32_e32 v82, v82
	v_exp_f32_e32 v83, v83
	v_pk_mul_f32 v[84:85], v[62:63], v[4:5] op_sel_hi:[0,1]
	v_exp_f32_e32 v84, v84
	v_exp_f32_e32 v85, v85
	v_pk_mul_f32 v[86:87], v[120:121], v[94:95] op_sel_hi:[0,1]
	v_pk_fma_f32 v[116:117], v[116:117], v[82:83], v[86:87]
	v_pk_mul_f32 v[82:83], v[120:121], v[96:97] op_sel_hi:[0,1]
	v_pk_fma_f32 v[118:119], v[118:119], v[84:85], v[82:83]
	s_nop 0
	s_waitcnt lgkmcnt(0)
	s_nop 0
	ds_read_b128 v[82:85], v19 offset:64
	ds_read_b128 v[86:89], v19 offset:80
	ds_read_b128 v[90:93], v19 offset:96
	ds_read_b128 v[94:97], v19 offset:112
	v_mov_b32_e32 v19, 0xb450
	v_pk_mul_f32 v[134:135], v[64:65], v[14:15] op_sel_hi:[0,1]
	v_exp_f32_e32 v134, v134
	v_exp_f32_e32 v135, v135
	v_pk_mul_f32 v[136:137], v[64:65], v[16:17] op_sel_hi:[0,1]
	v_exp_f32_e32 v136, v136
	v_exp_f32_e32 v137, v137
	v_mul_f32_e32 v120, v64, v61
	v_pk_mul_f32 v[98:99], v[120:121], v[98:99] op_sel_hi:[0,1]
	v_pk_fma_f32 v[122:123], v[122:123], v[134:135], v[98:99]
	v_pk_mul_f32 v[98:99], v[120:121], v[100:101] op_sel_hi:[0,1]
	v_pk_fma_f32 v[124:125], v[124:125], v[136:137], v[98:99]
	v_pk_mul_f32 v[98:99], v[64:65], v[10:11] op_sel_hi:[0,1]
	v_exp_f32_e32 v98, v98
	v_exp_f32_e32 v99, v99
	v_pk_mul_f32 v[100:101], v[64:65], v[12:13] op_sel_hi:[0,1]
	v_exp_f32_e32 v100, v100
	v_exp_f32_e32 v101, v101
	v_pk_mul_f32 v[102:103], v[120:121], v[102:103] op_sel_hi:[0,1]
	v_pk_fma_f32 v[128:129], v[128:129], v[98:99], v[102:103]
	v_pk_mul_f32 v[98:99], v[120:121], v[104:105] op_sel_hi:[0,1]
	v_pk_fma_f32 v[126:127], v[126:127], v[100:101], v[98:99]
	v_pk_mul_f32 v[98:99], v[64:65], v[6:7] op_sel_hi:[0,1]
	v_exp_f32_e32 v98, v98
	v_exp_f32_e32 v99, v99
	v_pk_mul_f32 v[100:101], v[64:65], v[8:9] op_sel_hi:[0,1]
	v_exp_f32_e32 v100, v100
	v_exp_f32_e32 v101, v101
	v_pk_mul_f32 v[102:103], v[120:121], v[108:109] op_sel_hi:[0,1]
	v_pk_fma_f32 v[130:131], v[130:131], v[98:99], v[102:103]
	v_pk_mul_f32 v[98:99], v[120:121], v[110:111] op_sel_hi:[0,1]
	v_pk_fma_f32 v[132:133], v[132:133], v[100:101], v[98:99]
	v_pk_mul_f32 v[98:99], v[64:65], v[2:3] op_sel_hi:[0,1]
	v_exp_f32_e32 v98, v98
	v_exp_f32_e32 v99, v99
	v_pk_mul_f32 v[100:101], v[64:65], v[4:5] op_sel_hi:[0,1]
	v_exp_f32_e32 v100, v100
	v_exp_f32_e32 v101, v101
	v_pk_mul_f32 v[102:103], v[120:121], v[112:113] op_sel_hi:[0,1]
	v_pk_fma_f32 v[116:117], v[116:117], v[98:99], v[102:103]
	v_pk_mul_f32 v[98:99], v[120:121], v[114:115] op_sel_hi:[0,1]
	v_pk_fma_f32 v[118:119], v[118:119], v[100:101], v[98:99]
	s_nop 0
	s_waitcnt lgkmcnt(0)
	s_nop 0
	ds_read_b128 v[98:101], v19 offset:64
	ds_read_b128 v[102:105], v19 offset:80
	ds_read_b128 v[108:111], v19 offset:96
	ds_read_b128 v[112:115], v19 offset:112
	v_mov_b32_e32 v19, 0xb520
	v_pk_mul_f32 v[134:135], v[66:67], v[14:15] op_sel_hi:[0,1]
	v_exp_f32_e32 v134, v134
	v_exp_f32_e32 v135, v135
	v_pk_mul_f32 v[136:137], v[66:67], v[16:17] op_sel_hi:[0,1]
	v_exp_f32_e32 v136, v136
	v_exp_f32_e32 v137, v137
	v_mul_f32_e32 v120, v66, v59
	v_pk_mul_f32 v[82:83], v[120:121], v[82:83] op_sel_hi:[0,1]
	v_pk_fma_f32 v[122:123], v[122:123], v[134:135], v[82:83]
	v_pk_mul_f32 v[82:83], v[120:121], v[84:85] op_sel_hi:[0,1]
	v_pk_fma_f32 v[124:125], v[124:125], v[136:137], v[82:83]
	v_pk_mul_f32 v[82:83], v[66:67], v[10:11] op_sel_hi:[0,1]
	v_exp_f32_e32 v82, v82
	v_exp_f32_e32 v83, v83
	v_pk_mul_f32 v[84:85], v[66:67], v[12:13] op_sel_hi:[0,1]
	v_exp_f32_e32 v84, v84
	v_exp_f32_e32 v85, v85
	v_pk_mul_f32 v[86:87], v[120:121], v[86:87] op_sel_hi:[0,1]
	v_pk_fma_f32 v[128:129], v[128:129], v[82:83], v[86:87]
	v_pk_mul_f32 v[82:83], v[120:121], v[88:89] op_sel_hi:[0,1]
	v_pk_fma_f32 v[126:127], v[126:127], v[84:85], v[82:83]
	v_pk_mul_f32 v[82:83], v[66:67], v[6:7] op_sel_hi:[0,1]
	v_exp_f32_e32 v82, v82
	v_exp_f32_e32 v83, v83
	v_pk_mul_f32 v[84:85], v[66:67], v[8:9] op_sel_hi:[0,1]
	v_exp_f32_e32 v84, v84
	v_exp_f32_e32 v85, v85
	v_pk_mul_f32 v[86:87], v[120:121], v[90:91] op_sel_hi:[0,1]
	v_pk_fma_f32 v[130:131], v[130:131], v[82:83], v[86:87]
	v_pk_mul_f32 v[82:83], v[120:121], v[92:93] op_sel_hi:[0,1]
	v_pk_fma_f32 v[132:133], v[132:133], v[84:85], v[82:83]
	v_pk_mul_f32 v[82:83], v[66:67], v[2:3] op_sel_hi:[0,1]
	v_exp_f32_e32 v82, v82
	v_exp_f32_e32 v83, v83
	v_pk_mul_f32 v[84:85], v[66:67], v[4:5] op_sel_hi:[0,1]
	v_exp_f32_e32 v84, v84
	v_exp_f32_e32 v85, v85
	v_pk_mul_f32 v[86:87], v[120:121], v[94:95] op_sel_hi:[0,1]
	v_pk_fma_f32 v[116:117], v[116:117], v[82:83], v[86:87]
	v_pk_mul_f32 v[82:83], v[120:121], v[96:97] op_sel_hi:[0,1]
	v_pk_fma_f32 v[118:119], v[118:119], v[84:85], v[82:83]
	s_nop 0
	s_waitcnt lgkmcnt(0)
	s_nop 0
	ds_read_b128 v[82:85], v19 offset:64
	ds_read_b128 v[86:89], v19 offset:80
	ds_read_b128 v[90:93], v19 offset:96
	ds_read_b128 v[94:97], v19 offset:112
	v_mov_b32_e32 v19, 0xb5f0
	v_pk_mul_f32 v[134:135], v[68:69], v[14:15] op_sel_hi:[0,1]
	v_exp_f32_e32 v134, v134
	v_exp_f32_e32 v135, v135
	v_pk_mul_f32 v[136:137], v[68:69], v[16:17] op_sel_hi:[0,1]
	v_exp_f32_e32 v136, v136
	v_exp_f32_e32 v137, v137
	v_mul_f32_e32 v120, v68, v57
	v_pk_mul_f32 v[98:99], v[120:121], v[98:99] op_sel_hi:[0,1]
	v_pk_fma_f32 v[122:123], v[122:123], v[134:135], v[98:99]
	v_pk_mul_f32 v[98:99], v[120:121], v[100:101] op_sel_hi:[0,1]
	v_pk_fma_f32 v[124:125], v[124:125], v[136:137], v[98:99]
	v_pk_mul_f32 v[98:99], v[68:69], v[10:11] op_sel_hi:[0,1]
	v_exp_f32_e32 v98, v98
	v_exp_f32_e32 v99, v99
	v_pk_mul_f32 v[100:101], v[68:69], v[12:13] op_sel_hi:[0,1]
	v_exp_f32_e32 v100, v100
	v_exp_f32_e32 v101, v101
	v_pk_mul_f32 v[102:103], v[120:121], v[102:103] op_sel_hi:[0,1]
	v_pk_fma_f32 v[128:129], v[128:129], v[98:99], v[102:103]
	v_pk_mul_f32 v[98:99], v[120:121], v[104:105] op_sel_hi:[0,1]
	v_pk_fma_f32 v[126:127], v[126:127], v[100:101], v[98:99]
	v_pk_mul_f32 v[98:99], v[68:69], v[6:7] op_sel_hi:[0,1]
	v_exp_f32_e32 v98, v98
	v_exp_f32_e32 v99, v99
	v_pk_mul_f32 v[100:101], v[68:69], v[8:9] op_sel_hi:[0,1]
	v_exp_f32_e32 v100, v100
	v_exp_f32_e32 v101, v101
	v_pk_mul_f32 v[102:103], v[120:121], v[108:109] op_sel_hi:[0,1]
	v_pk_fma_f32 v[130:131], v[130:131], v[98:99], v[102:103]
	v_pk_mul_f32 v[98:99], v[120:121], v[110:111] op_sel_hi:[0,1]
	v_pk_fma_f32 v[132:133], v[132:133], v[100:101], v[98:99]
	v_pk_mul_f32 v[98:99], v[68:69], v[2:3] op_sel_hi:[0,1]
	v_exp_f32_e32 v98, v98
	v_exp_f32_e32 v99, v99
	v_pk_mul_f32 v[100:101], v[68:69], v[4:5] op_sel_hi:[0,1]
	v_exp_f32_e32 v100, v100
	v_exp_f32_e32 v101, v101
	v_pk_mul_f32 v[102:103], v[120:121], v[112:113] op_sel_hi:[0,1]
	v_pk_fma_f32 v[116:117], v[116:117], v[98:99], v[102:103]
	v_pk_mul_f32 v[98:99], v[120:121], v[114:115] op_sel_hi:[0,1]
	v_pk_fma_f32 v[118:119], v[118:119], v[100:101], v[98:99]
	s_nop 0
	s_waitcnt lgkmcnt(0)
	s_nop 0
	ds_read_b128 v[98:101], v19 offset:64
	ds_read_b128 v[102:105], v19 offset:80
	ds_read_b128 v[108:111], v19 offset:96
	ds_read_b128 v[112:115], v19 offset:112
	v_mov_b32_e32 v19, 0xb6c0
	v_pk_mul_f32 v[134:135], v[70:71], v[14:15] op_sel_hi:[0,1]
	v_exp_f32_e32 v134, v134
	v_exp_f32_e32 v135, v135
	v_pk_mul_f32 v[136:137], v[70:71], v[16:17] op_sel_hi:[0,1]
	v_exp_f32_e32 v136, v136
	v_exp_f32_e32 v137, v137
	v_mul_f32_e32 v120, v70, v55
	v_pk_mul_f32 v[82:83], v[120:121], v[82:83] op_sel_hi:[0,1]
	v_pk_fma_f32 v[122:123], v[122:123], v[134:135], v[82:83]
	v_pk_mul_f32 v[82:83], v[120:121], v[84:85] op_sel_hi:[0,1]
	v_pk_fma_f32 v[124:125], v[124:125], v[136:137], v[82:83]
	v_pk_mul_f32 v[82:83], v[70:71], v[10:11] op_sel_hi:[0,1]
	v_exp_f32_e32 v82, v82
	v_exp_f32_e32 v83, v83
	v_pk_mul_f32 v[84:85], v[70:71], v[12:13] op_sel_hi:[0,1]
	v_exp_f32_e32 v84, v84
	v_exp_f32_e32 v85, v85
	v_pk_mul_f32 v[86:87], v[120:121], v[86:87] op_sel_hi:[0,1]
	v_pk_fma_f32 v[128:129], v[128:129], v[82:83], v[86:87]
	v_pk_mul_f32 v[82:83], v[120:121], v[88:89] op_sel_hi:[0,1]
	v_pk_fma_f32 v[126:127], v[126:127], v[84:85], v[82:83]
	v_pk_mul_f32 v[82:83], v[70:71], v[6:7] op_sel_hi:[0,1]
	v_exp_f32_e32 v82, v82
	v_exp_f32_e32 v83, v83
	v_pk_mul_f32 v[84:85], v[70:71], v[8:9] op_sel_hi:[0,1]
	v_exp_f32_e32 v84, v84
	v_exp_f32_e32 v85, v85
	v_pk_mul_f32 v[86:87], v[120:121], v[90:91] op_sel_hi:[0,1]
	v_pk_fma_f32 v[130:131], v[130:131], v[82:83], v[86:87]
	v_pk_mul_f32 v[82:83], v[120:121], v[92:93] op_sel_hi:[0,1]
	v_pk_fma_f32 v[132:133], v[132:133], v[84:85], v[82:83]
	v_pk_mul_f32 v[82:83], v[70:71], v[2:3] op_sel_hi:[0,1]
	v_exp_f32_e32 v82, v82
	v_exp_f32_e32 v83, v83
	v_pk_mul_f32 v[84:85], v[70:71], v[4:5] op_sel_hi:[0,1]
	v_exp_f32_e32 v84, v84
	v_exp_f32_e32 v85, v85
	v_pk_mul_f32 v[86:87], v[120:121], v[94:95] op_sel_hi:[0,1]
	v_pk_fma_f32 v[116:117], v[116:117], v[82:83], v[86:87]
	v_pk_mul_f32 v[82:83], v[120:121], v[96:97] op_sel_hi:[0,1]
	v_pk_fma_f32 v[118:119], v[118:119], v[84:85], v[82:83]
	s_nop 0
	s_waitcnt lgkmcnt(0)
	s_nop 0
	ds_read_b128 v[82:85], v19 offset:64
	ds_read_b128 v[86:89], v19 offset:80
	ds_read_b128 v[90:93], v19 offset:96
	ds_read_b128 v[94:97], v19 offset:112
	v_mov_b32_e32 v19, 0xb790
	v_pk_mul_f32 v[134:135], v[72:73], v[14:15] op_sel_hi:[0,1]
	v_exp_f32_e32 v134, v134
	v_exp_f32_e32 v135, v135
	v_pk_mul_f32 v[136:137], v[72:73], v[16:17] op_sel_hi:[0,1]
	v_exp_f32_e32 v136, v136
	v_exp_f32_e32 v137, v137
	v_mul_f32_e32 v120, v72, v53
	v_pk_mul_f32 v[98:99], v[120:121], v[98:99] op_sel_hi:[0,1]
	v_pk_fma_f32 v[122:123], v[122:123], v[134:135], v[98:99]
	v_pk_mul_f32 v[98:99], v[120:121], v[100:101] op_sel_hi:[0,1]
	v_pk_fma_f32 v[124:125], v[124:125], v[136:137], v[98:99]
	v_pk_mul_f32 v[98:99], v[72:73], v[10:11] op_sel_hi:[0,1]
	v_exp_f32_e32 v98, v98
	v_exp_f32_e32 v99, v99
	v_pk_mul_f32 v[100:101], v[72:73], v[12:13] op_sel_hi:[0,1]
	v_exp_f32_e32 v100, v100
	v_exp_f32_e32 v101, v101
	v_pk_mul_f32 v[102:103], v[120:121], v[102:103] op_sel_hi:[0,1]
	v_pk_fma_f32 v[128:129], v[128:129], v[98:99], v[102:103]
	v_pk_mul_f32 v[98:99], v[120:121], v[104:105] op_sel_hi:[0,1]
	v_pk_fma_f32 v[126:127], v[126:127], v[100:101], v[98:99]
	v_pk_mul_f32 v[98:99], v[72:73], v[6:7] op_sel_hi:[0,1]
	v_exp_f32_e32 v98, v98
	v_exp_f32_e32 v99, v99
	v_pk_mul_f32 v[100:101], v[72:73], v[8:9] op_sel_hi:[0,1]
	v_exp_f32_e32 v100, v100
	v_exp_f32_e32 v101, v101
	v_pk_mul_f32 v[102:103], v[120:121], v[108:109] op_sel_hi:[0,1]
	v_pk_fma_f32 v[130:131], v[130:131], v[98:99], v[102:103]
	v_pk_mul_f32 v[98:99], v[120:121], v[110:111] op_sel_hi:[0,1]
	v_pk_fma_f32 v[132:133], v[132:133], v[100:101], v[98:99]
	v_pk_mul_f32 v[98:99], v[72:73], v[2:3] op_sel_hi:[0,1]
	v_exp_f32_e32 v98, v98
	v_exp_f32_e32 v99, v99
	v_pk_mul_f32 v[100:101], v[72:73], v[4:5] op_sel_hi:[0,1]
	v_exp_f32_e32 v100, v100
	v_exp_f32_e32 v101, v101
	v_pk_mul_f32 v[102:103], v[120:121], v[112:113] op_sel_hi:[0,1]
	v_pk_fma_f32 v[116:117], v[116:117], v[98:99], v[102:103]
	v_pk_mul_f32 v[98:99], v[120:121], v[114:115] op_sel_hi:[0,1]
	v_pk_fma_f32 v[118:119], v[118:119], v[100:101], v[98:99]
	s_nop 0
	s_waitcnt lgkmcnt(0)
	s_nop 0
	ds_read_b128 v[98:101], v19 offset:64
	ds_read_b128 v[102:105], v19 offset:80
	ds_read_b128 v[108:111], v19 offset:96
	ds_read_b128 v[112:115], v19 offset:112
	v_mov_b32_e32 v19, 0xb860
	v_pk_mul_f32 v[134:135], v[74:75], v[14:15] op_sel_hi:[0,1]
	v_exp_f32_e32 v134, v134
	v_exp_f32_e32 v135, v135
	v_pk_mul_f32 v[136:137], v[74:75], v[16:17] op_sel_hi:[0,1]
	v_exp_f32_e32 v136, v136
	v_exp_f32_e32 v137, v137
	v_mul_f32_e32 v120, v74, v51
	v_pk_mul_f32 v[82:83], v[120:121], v[82:83] op_sel_hi:[0,1]
	v_pk_fma_f32 v[122:123], v[122:123], v[134:135], v[82:83]
	v_pk_mul_f32 v[82:83], v[120:121], v[84:85] op_sel_hi:[0,1]
	v_pk_fma_f32 v[124:125], v[124:125], v[136:137], v[82:83]
	v_pk_mul_f32 v[82:83], v[74:75], v[10:11] op_sel_hi:[0,1]
	v_exp_f32_e32 v82, v82
	v_exp_f32_e32 v83, v83
	v_pk_mul_f32 v[84:85], v[74:75], v[12:13] op_sel_hi:[0,1]
	v_exp_f32_e32 v84, v84
	v_exp_f32_e32 v85, v85
	v_pk_mul_f32 v[86:87], v[120:121], v[86:87] op_sel_hi:[0,1]
	v_pk_fma_f32 v[128:129], v[128:129], v[82:83], v[86:87]
	v_pk_mul_f32 v[82:83], v[120:121], v[88:89] op_sel_hi:[0,1]
	v_pk_fma_f32 v[126:127], v[126:127], v[84:85], v[82:83]
	v_pk_mul_f32 v[82:83], v[74:75], v[6:7] op_sel_hi:[0,1]
	v_exp_f32_e32 v82, v82
	v_exp_f32_e32 v83, v83
	v_pk_mul_f32 v[84:85], v[74:75], v[8:9] op_sel_hi:[0,1]
	v_exp_f32_e32 v84, v84
	v_exp_f32_e32 v85, v85
	v_pk_mul_f32 v[86:87], v[120:121], v[90:91] op_sel_hi:[0,1]
	v_pk_fma_f32 v[130:131], v[130:131], v[82:83], v[86:87]
	v_pk_mul_f32 v[82:83], v[120:121], v[92:93] op_sel_hi:[0,1]
	v_pk_fma_f32 v[132:133], v[132:133], v[84:85], v[82:83]
	v_pk_mul_f32 v[82:83], v[74:75], v[2:3] op_sel_hi:[0,1]
	v_exp_f32_e32 v82, v82
	v_exp_f32_e32 v83, v83
	v_pk_mul_f32 v[84:85], v[74:75], v[4:5] op_sel_hi:[0,1]
	v_exp_f32_e32 v84, v84
	v_exp_f32_e32 v85, v85
	v_pk_mul_f32 v[86:87], v[120:121], v[94:95] op_sel_hi:[0,1]
	v_pk_fma_f32 v[116:117], v[116:117], v[82:83], v[86:87]
	v_pk_mul_f32 v[82:83], v[120:121], v[96:97] op_sel_hi:[0,1]
	v_pk_fma_f32 v[118:119], v[118:119], v[84:85], v[82:83]
	s_nop 0
	s_waitcnt lgkmcnt(0)
	s_nop 0
	ds_read_b128 v[82:85], v19 offset:64
	ds_read_b128 v[86:89], v19 offset:80
	ds_read_b128 v[90:93], v19 offset:96
	ds_read_b128 v[94:97], v19 offset:112
	v_mov_b32_e32 v19, 0xb930
	v_pk_mul_f32 v[134:135], v[76:77], v[14:15] op_sel_hi:[0,1]
	v_exp_f32_e32 v134, v134
	v_exp_f32_e32 v135, v135
	v_pk_mul_f32 v[136:137], v[76:77], v[16:17] op_sel_hi:[0,1]
	v_exp_f32_e32 v136, v136
	v_exp_f32_e32 v137, v137
	v_mul_f32_e32 v120, v76, v49
	v_pk_mul_f32 v[98:99], v[120:121], v[98:99] op_sel_hi:[0,1]
	v_pk_fma_f32 v[122:123], v[122:123], v[134:135], v[98:99]
	v_pk_mul_f32 v[98:99], v[120:121], v[100:101] op_sel_hi:[0,1]
	v_pk_fma_f32 v[124:125], v[124:125], v[136:137], v[98:99]
	v_pk_mul_f32 v[98:99], v[76:77], v[10:11] op_sel_hi:[0,1]
	v_exp_f32_e32 v98, v98
	v_exp_f32_e32 v99, v99
	v_pk_mul_f32 v[100:101], v[76:77], v[12:13] op_sel_hi:[0,1]
	v_exp_f32_e32 v100, v100
	v_exp_f32_e32 v101, v101
	v_pk_mul_f32 v[102:103], v[120:121], v[102:103] op_sel_hi:[0,1]
	v_pk_fma_f32 v[128:129], v[128:129], v[98:99], v[102:103]
	v_pk_mul_f32 v[98:99], v[120:121], v[104:105] op_sel_hi:[0,1]
	v_pk_fma_f32 v[126:127], v[126:127], v[100:101], v[98:99]
	v_pk_mul_f32 v[98:99], v[76:77], v[6:7] op_sel_hi:[0,1]
	v_exp_f32_e32 v98, v98
	v_exp_f32_e32 v99, v99
	v_pk_mul_f32 v[100:101], v[76:77], v[8:9] op_sel_hi:[0,1]
	v_exp_f32_e32 v100, v100
	v_exp_f32_e32 v101, v101
	v_pk_mul_f32 v[102:103], v[120:121], v[108:109] op_sel_hi:[0,1]
	v_pk_fma_f32 v[130:131], v[130:131], v[98:99], v[102:103]
	v_pk_mul_f32 v[98:99], v[120:121], v[110:111] op_sel_hi:[0,1]
	v_pk_fma_f32 v[132:133], v[132:133], v[100:101], v[98:99]
	v_pk_mul_f32 v[98:99], v[76:77], v[2:3] op_sel_hi:[0,1]
	v_exp_f32_e32 v98, v98
	v_exp_f32_e32 v99, v99
	v_pk_mul_f32 v[100:101], v[76:77], v[4:5] op_sel_hi:[0,1]
	v_exp_f32_e32 v100, v100
	v_exp_f32_e32 v101, v101
	v_pk_mul_f32 v[102:103], v[120:121], v[112:113] op_sel_hi:[0,1]
	v_pk_fma_f32 v[116:117], v[116:117], v[98:99], v[102:103]
	v_pk_mul_f32 v[98:99], v[120:121], v[114:115] op_sel_hi:[0,1]
	v_pk_fma_f32 v[118:119], v[118:119], v[100:101], v[98:99]
	s_nop 0
	s_waitcnt lgkmcnt(0)
	s_nop 0
	ds_read_b128 v[98:101], v19 offset:64
	ds_read_b128 v[102:105], v19 offset:80
	ds_read_b128 v[108:111], v19 offset:96
	ds_read_b128 v[112:115], v19 offset:112
	v_add_f32_e32 v19, 0, v80
	v_add_f32_e32 v19, v19, v20
	v_add_f32_e32 v19, v19, v22
	v_add_f32_e32 v19, v19, v24
	v_add_f32_e32 v19, v19, v26
	v_add_f32_e32 v19, v19, v28
	v_add_f32_e32 v19, v19, v30
	v_add_f32_e32 v19, v19, v32
	v_add_f32_e32 v19, v19, v34
	v_add_f32_e32 v19, v19, v36
	v_pk_mul_f32 v[134:135], v[78:79], v[14:15] op_sel_hi:[0,1]
	v_pk_mul_f32 v[136:137], v[78:79], v[16:17] op_sel_hi:[0,1]
	v_add_f32_e32 v19, v19, v38
	v_exp_f32_e32 v134, v134
	v_exp_f32_e32 v135, v135
	v_exp_f32_e32 v136, v136
	v_exp_f32_e32 v137, v137
	v_add_f32_e32 v19, v19, v40
	v_add_f32_e32 v19, v19, v42
	v_mul_f32_e32 v120, v78, v47
	v_add_f32_e32 v19, v19, v44
	v_pk_mul_f32 v[82:83], v[120:121], v[82:83] op_sel_hi:[0,1]
	v_pk_mul_f32 v[84:85], v[120:121], v[84:85] op_sel_hi:[0,1]
	v_add_f32_e32 v19, v19, v46
	v_pk_fma_f32 v[82:83], v[122:123], v[134:135], v[82:83]
	v_pk_fma_f32 v[84:85], v[124:125], v[136:137], v[84:85]
	v_pk_mul_f32 v[122:123], v[78:79], v[10:11] op_sel_hi:[0,1]
	v_pk_mul_f32 v[124:125], v[78:79], v[12:13] op_sel_hi:[0,1]
	v_add_f32_e32 v19, v19, v48
	v_exp_f32_e32 v122, v122
	v_exp_f32_e32 v123, v123
	v_exp_f32_e32 v124, v124
	v_exp_f32_e32 v125, v125
	v_add_f32_e32 v19, v19, v50
	v_add_f32_e32 v19, v19, v52
	v_add_f32_e32 v19, v19, v54
	v_pk_mul_f32 v[86:87], v[120:121], v[86:87] op_sel_hi:[0,1]
	v_pk_mul_f32 v[88:89], v[120:121], v[88:89] op_sel_hi:[0,1]
	v_add_f32_e32 v19, v19, v56
	v_pk_fma_f32 v[86:87], v[128:129], v[122:123], v[86:87]
	v_pk_fma_f32 v[88:89], v[126:127], v[124:125], v[88:89]
	v_pk_mul_f32 v[122:123], v[78:79], v[6:7] op_sel_hi:[0,1]
	v_pk_mul_f32 v[124:125], v[78:79], v[8:9] op_sel_hi:[0,1]
	v_add_f32_e32 v19, v19, v58
	v_exp_f32_e32 v122, v122
	v_exp_f32_e32 v123, v123
	v_exp_f32_e32 v124, v124
	v_exp_f32_e32 v125, v125
	v_add_f32_e32 v19, v19, v60
	v_add_f32_e32 v19, v19, v62
	v_add_f32_e32 v19, v19, v64
	v_pk_mul_f32 v[90:91], v[120:121], v[90:91] op_sel_hi:[0,1]
	v_pk_mul_f32 v[92:93], v[120:121], v[92:93] op_sel_hi:[0,1]
	v_add_f32_e32 v19, v19, v66
	v_pk_fma_f32 v[90:91], v[130:131], v[122:123], v[90:91]
	v_pk_fma_f32 v[92:93], v[132:133], v[124:125], v[92:93]
	v_pk_mul_f32 v[122:123], v[78:79], v[2:3] op_sel_hi:[0,1]
	v_pk_mul_f32 v[124:125], v[78:79], v[4:5] op_sel_hi:[0,1]
	v_add_f32_e32 v19, v19, v68
	v_exp_f32_e32 v122, v122
	v_exp_f32_e32 v123, v123
	v_exp_f32_e32 v124, v124
	v_exp_f32_e32 v125, v125
	v_add_f32_e32 v19, v19, v70
	v_add_f32_e32 v19, v19, v72
	v_add_f32_e32 v19, v19, v74
	v_pk_mul_f32 v[94:95], v[120:121], v[94:95] op_sel_hi:[0,1]
	v_pk_mul_f32 v[96:97], v[120:121], v[96:97] op_sel_hi:[0,1]
	v_add_f32_e32 v19, v19, v76
	v_pk_fma_f32 v[94:95], v[116:117], v[122:123], v[94:95]
	v_pk_fma_f32 v[96:97], v[118:119], v[124:125], v[96:97]
	v_add_f32_e32 v19, v19, v78
	s_waitcnt lgkmcnt(0)
	v_cvt_f32_f16_e32 v20, v106
	v_add_f32_e32 v19, v19, v18
	v_pk_mul_f32 v[4:5], v[18:19], v[4:5] op_sel_hi:[0,1]
	v_exp_f32_e32 v4, v4
	v_exp_f32_e32 v5, v5
	v_pk_mul_f32 v[14:15], v[18:19], v[14:15] op_sel_hi:[0,1]
	v_exp_f32_e32 v14, v14
	v_exp_f32_e32 v15, v15
	v_mul_f32_e32 v20, v18, v20
	v_pk_mul_f32 v[22:23], v[20:21], v[114:115] op_sel_hi:[0,1]
	v_pk_fma_f32 v[22:23], v[96:97], v[4:5], v[22:23]
	v_pk_mul_f32 v[4:5], v[20:21], v[98:99] op_sel_hi:[0,1]
	v_pk_fma_f32 v[14:15], v[82:83], v[14:15], v[4:5]
	v_pk_mul_f32 v[4:5], v[18:19], v[16:17] op_sel_hi:[0,1]
	v_exp_f32_e32 v4, v4
	v_exp_f32_e32 v5, v5
	v_pk_mul_f32 v[10:11], v[18:19], v[10:11] op_sel_hi:[0,1]
	v_exp_f32_e32 v10, v10
	v_exp_f32_e32 v11, v11
	v_pk_mul_f32 v[16:17], v[20:21], v[100:101] op_sel_hi:[0,1]
	v_pk_fma_f32 v[16:17], v[84:85], v[4:5], v[16:17]
	v_pk_mul_f32 v[4:5], v[20:21], v[102:103] op_sel_hi:[0,1]
	v_pk_fma_f32 v[10:11], v[86:87], v[10:11], v[4:5]
	v_pk_mul_f32 v[4:5], v[18:19], v[12:13] op_sel_hi:[0,1]
	v_exp_f32_e32 v4, v4
	v_exp_f32_e32 v5, v5
	v_pk_mul_f32 v[6:7], v[18:19], v[6:7] op_sel_hi:[0,1]
	v_exp_f32_e32 v6, v6
	v_exp_f32_e32 v7, v7
	v_pk_mul_f32 v[8:9], v[18:19], v[8:9] op_sel_hi:[0,1]
	v_exp_f32_e32 v8, v8
	v_exp_f32_e32 v9, v9
	v_pk_mul_f32 v[2:3], v[18:19], v[2:3] op_sel_hi:[0,1]
	v_pk_mul_f32 v[12:13], v[20:21], v[104:105] op_sel_hi:[0,1]
	v_exp_f32_e32 v2, v2
	v_exp_f32_e32 v3, v3
	v_pk_fma_f32 v[4:5], v[88:89], v[4:5], v[12:13]
	v_pk_mul_f32 v[12:13], v[20:21], v[108:109] op_sel_hi:[0,1]
	v_pk_fma_f32 v[6:7], v[90:91], v[6:7], v[12:13]
	v_pk_mul_f32 v[12:13], v[20:21], v[110:111] op_sel_hi:[0,1]
	v_pk_fma_f32 v[8:9], v[92:93], v[8:9], v[12:13]
	v_pk_mul_f32 v[12:13], v[20:21], v[112:113] op_sel_hi:[0,1]
	v_cvt_pk_f16_f32 v5, v4, v5
	v_cvt_pk_f16_f32 v4, v10, v11
	v_lshl_or_b32 v10, v0, 4, s6
	v_mov_b32_e32 v11, s7
	v_pk_fma_f32 v[12:13], v[94:95], v[2:3], v[12:13]
	v_cvt_pk_f16_f32 v3, v16, v17
	v_cvt_pk_f16_f32 v2, v14, v15
	v_lshl_add_u64 v[10:11], s[4:5], 0, v[10:11]
	s_movk_i32 s4, 0x2000
	global_store_dwordx4 v[10:11], v[2:5], off sc0 sc1
	global_store_dword v1, v19, s[0:1] sc0 sc1
	s_nop 0
	v_cvt_pk_f16_f32 v2, v6, v7
	v_add_co_u32_e32 v6, vcc, s4, v10
	v_cvt_pk_f16_f32 v5, v22, v23
	v_cvt_pk_f16_f32 v4, v12, v13
	v_cvt_pk_f16_f32 v3, v8, v9
	v_addc_co_u32_e32 v7, vcc, 0, v11, vcc
	global_store_dwordx4 v[6:7], v[2:5], off sc0 sc1
	s_endpgm
